# nt hint extended to the prologue's converted-weight stores and the final rowpass residual reads
# speedup vs baseline: 1.0025x; 1.0025x over previous
.LBB0_12:
	s_or_b64 exec, exec, s[24:25]
	v_add_u32_e32 v66, v189, v188
	s_waitcnt vmcnt(0)
	ds_write2_b32 v66, v6, v7 offset1:1
	ds_write2_b32 v66, v8, v9 offset0:2 offset1:3
	v_add_u32_e32 v6, 0x410, v66
	ds_write2_b32 v6, v2, v3 offset1:1
	v_add_u32_e32 v2, 0x418, v66
	ds_write2_b32 v2, v4, v5 offset1:1
	v_add_u32_e32 v2, 0x820, v66
	ds_write2_b32 v2, v14, v15 offset1:1
	v_add_u32_e32 v2, 0x828, v66
	ds_write2_b32 v2, v16, v17 offset1:1
	v_add_u32_e32 v2, 0xc30, v66
	ds_write2_b32 v2, v10, v11 offset1:1
	v_add_u32_e32 v2, 0xc38, v66
	ds_write2_b32 v2, v12, v13 offset1:1
	v_add_u32_e32 v2, 0x1040, v66
	ds_write2_b32 v2, v22, v23 offset1:1
	v_add_u32_e32 v2, 0x1048, v66
	ds_write2_b32 v2, v24, v25 offset1:1
	v_add_u32_e32 v2, 0x1450, v66
	ds_write2_b32 v2, v18, v19 offset1:1
	v_add_u32_e32 v2, 0x1458, v66
	ds_write2_b32 v2, v20, v21 offset1:1
	v_add_u32_e32 v2, 0x1860, v66
	ds_write2_b32 v2, v30, v31 offset1:1
	v_add_u32_e32 v2, 0x1868, v66
	ds_write2_b32 v2, v32, v33 offset1:1
	v_add_u32_e32 v2, 0x1c70, v66
	ds_write2_b32 v2, v26, v27 offset1:1
	v_add_u32_e32 v2, 0x1c78, v66
	ds_write2_b32 v2, v28, v29 offset1:1
	v_add_u32_e32 v2, 0x2080, v66
	ds_write2_b32 v2, v38, v39 offset1:1
	v_add_u32_e32 v2, 0x2088, v66
	ds_write2_b32 v2, v40, v41 offset1:1
	v_add_u32_e32 v2, 0x2490, v66
	ds_write2_b32 v2, v34, v35 offset1:1
	v_add_u32_e32 v2, 0x2498, v66
	ds_write2_b32 v2, v36, v37 offset1:1
	v_add_u32_e32 v2, 0x28a0, v66
	ds_write2_b32 v2, v46, v47 offset1:1
	v_add_u32_e32 v2, 0x28a8, v66
	ds_write2_b32 v2, v48, v49 offset1:1
	v_add_u32_e32 v2, 0x2cb0, v66
	ds_write2_b32 v2, v42, v43 offset1:1
	v_add_u32_e32 v2, 0x2cb8, v66
	ds_write2_b32 v2, v44, v45 offset1:1
	v_add_u32_e32 v2, 0x30c0, v66
	ds_write2_b32 v2, v54, v55 offset1:1
	v_add_u32_e32 v2, 0x30c8, v66
	ds_write2_b32 v2, v56, v57 offset1:1
	v_add_u32_e32 v2, 0x34d0, v66
	ds_write2_b32 v2, v50, v51 offset1:1
	v_add_u32_e32 v2, 0x34d8, v66
	ds_write2_b32 v2, v52, v53 offset1:1
	v_add_u32_e32 v2, 0x38e0, v66
	ds_write2_b32 v2, v62, v63 offset1:1
	v_add_u32_e32 v2, 0x38e8, v66
	ds_write2_b32 v2, v64, v65 offset1:1
	v_add_u32_e32 v2, 0x3cf0, v66
	s_mul_hi_i32 s2, s16, 0xe00000
	s_mul_i32 s16, s16, 0xe00000
	ds_write2_b32 v2, v58, v59 offset1:1
	v_add_u32_e32 v2, 0x3cf8, v66
	s_add_u32 s20, s42, s16
	ds_write2_b32 v2, v60, v61 offset1:1
	s_addc_u32 s2, s43, s2
	s_ashr_i32 s19, s18, 31
	s_waitcnt lgkmcnt(0)
	s_lshl_b64 s[16:17], s[18:19], 11
	v_add_u32_e32 v26, 0x400, v185
	s_add_u32 s18, s20, s16
	ds_read2_b32 v[6:7], v185 offset0:65 offset1:73
	ds_read2_b32 v[8:9], v185 offset1:8
	ds_read2_b32 v[10:11], v185 offset0:130 offset1:138
	ds_read2_b32 v[12:13], v185 offset0:195 offset1:203
	ds_read2_b32 v[14:15], v26 offset0:4 offset1:12
	ds_read2_b32 v[16:17], v26 offset0:69 offset1:77
	ds_read2_b32 v[18:19], v26 offset0:134 offset1:142
	ds_read2_b32 v[20:21], v26 offset0:199 offset1:207
	s_addc_u32 s2, s2, s17
	s_lshl_b64 s[16:17], s[22:23], 1
	s_add_u32 s16, s18, s16
	s_addc_u32 s17, s2, s17
	v_lshlrev_b32_e32 v66, 1, v70
	v_lshl_add_u64 v[22:23], s[16:17], 0, v[66:67]
	s_waitcnt lgkmcnt(6)
	v_cvt_pk_bf16_f32 v2, v8, v6
	s_waitcnt lgkmcnt(4)
	v_cvt_pk_bf16_f32 v3, v10, v12
	s_waitcnt lgkmcnt(2)
	v_cvt_pk_bf16_f32 v4, v14, v16
	s_waitcnt lgkmcnt(0)
	v_cvt_pk_bf16_f32 v5, v18, v20
	v_lshl_add_u64 v[24:25], v[22:23], 0, v[112:113]
	global_store_dwordx4 v[24:25], v[2:5], off nt
	s_nop 1
	v_cvt_pk_bf16_f32 v2, v9, v7
	v_cvt_pk_bf16_f32 v3, v11, v13
	v_cvt_pk_bf16_f32 v4, v15, v17
	v_cvt_pk_bf16_f32 v5, v19, v21
	ds_read2_b32 v[8:9], v185 offset0:81 offset1:89
	ds_read2_b32 v[10:11], v185 offset0:16 offset1:24
	ds_read2_b32 v[12:13], v185 offset0:146 offset1:154
	ds_read2_b32 v[14:15], v185 offset0:211 offset1:219
	ds_read2_b32 v[16:17], v26 offset0:20 offset1:28
	ds_read2_b32 v[18:19], v26 offset0:85 offset1:93
	ds_read2_b32 v[20:21], v26 offset0:150 offset1:158
	ds_read2_b32 v[24:25], v26 offset0:215 offset1:223
	v_lshl_add_u64 v[6:7], v[22:23], 0, v[74:75]
	global_store_dwordx4 v[6:7], v[2:5], off nt
	v_lshl_add_u64 v[6:7], v[22:23], 0, v[80:81]
	s_waitcnt lgkmcnt(6)
	v_cvt_pk_bf16_f32 v2, v10, v8
	s_waitcnt lgkmcnt(4)
	v_cvt_pk_bf16_f32 v3, v12, v14
	s_waitcnt lgkmcnt(2)
	v_cvt_pk_bf16_f32 v4, v16, v18
	s_waitcnt lgkmcnt(0)
	v_cvt_pk_bf16_f32 v5, v20, v24
	global_store_dwordx4 v[6:7], v[2:5], off nt
	v_lshl_add_u64 v[6:7], v[22:23], 0, v[86:87]
	s_nop 0
	v_cvt_pk_bf16_f32 v2, v11, v9
	v_cvt_pk_bf16_f32 v3, v13, v15
	v_cvt_pk_bf16_f32 v4, v17, v19
	v_cvt_pk_bf16_f32 v5, v21, v25
	ds_read2_b32 v[8:9], v185 offset0:32 offset1:40
	ds_read2_b32 v[10:11], v185 offset0:97 offset1:105
	ds_read2_b32 v[12:13], v185 offset0:162 offset1:170
	ds_read2_b32 v[14:15], v185 offset0:227 offset1:235
	ds_read2_b32 v[16:17], v26 offset0:36 offset1:44
	ds_read2_b32 v[18:19], v26 offset0:101 offset1:109
	ds_read2_b32 v[20:21], v26 offset0:166 offset1:174
	ds_read2_b32 v[24:25], v26 offset0:231 offset1:239
	global_store_dwordx4 v[6:7], v[2:5], off nt
	v_lshl_add_u64 v[6:7], v[22:23], 0, v[90:91]
	s_waitcnt lgkmcnt(6)
	v_cvt_pk_bf16_f32 v2, v8, v10
	s_waitcnt lgkmcnt(4)
	v_cvt_pk_bf16_f32 v3, v12, v14
	s_waitcnt lgkmcnt(2)
	v_cvt_pk_bf16_f32 v4, v16, v18
	s_waitcnt lgkmcnt(0)
	v_cvt_pk_bf16_f32 v5, v20, v24
	global_store_dwordx4 v[6:7], v[2:5], off nt
	v_lshl_add_u64 v[6:7], v[22:23], 0, v[94:95]
	s_nop 0
	v_cvt_pk_bf16_f32 v2, v9, v11
	v_cvt_pk_bf16_f32 v3, v13, v15
	v_cvt_pk_bf16_f32 v4, v17, v19
	v_cvt_pk_bf16_f32 v5, v21, v25
	ds_read2_b32 v[8:9], v185 offset0:48 offset1:56
	ds_read2_b32 v[10:11], v185 offset0:113 offset1:121
	ds_read2_b32 v[12:13], v185 offset0:178 offset1:186
	ds_read2_b32 v[14:15], v185 offset0:243 offset1:251
	ds_read2_b32 v[16:17], v26 offset0:52 offset1:60
	ds_read2_b32 v[18:19], v26 offset0:117 offset1:125
	ds_read2_b32 v[20:21], v26 offset0:182 offset1:190
	ds_read2_b32 v[24:25], v26 offset0:247 offset1:255
	global_store_dwordx4 v[6:7], v[2:5], off nt
	v_lshl_add_u64 v[6:7], v[22:23], 0, v[98:99]
	s_waitcnt lgkmcnt(6)
	v_cvt_pk_bf16_f32 v2, v8, v10
	s_waitcnt lgkmcnt(4)
	v_cvt_pk_bf16_f32 v3, v12, v14
	s_waitcnt lgkmcnt(2)
	v_cvt_pk_bf16_f32 v4, v16, v18
	s_waitcnt lgkmcnt(0)
	v_cvt_pk_bf16_f32 v5, v20, v24
	global_store_dwordx4 v[6:7], v[2:5], off nt
	v_lshl_add_u64 v[6:7], v[22:23], 0, v[102:103]
	s_nop 0
	v_cvt_pk_bf16_f32 v2, v9, v11
	v_cvt_pk_bf16_f32 v3, v13, v15
	v_cvt_pk_bf16_f32 v4, v17, v19
	v_cvt_pk_bf16_f32 v5, v21, v25
	global_store_dwordx4 v[6:7], v[2:5], off nt
	s_waitcnt lgkmcnt(0)

.LBB0_14:
	s_mul_hi_i32 s2, s30, 0x9c09c09d
	s_add_i32 s2, s2, s30
	s_lshr_b32 s16, s2, 31
	s_ashr_i32 s2, s2, 14
	s_add_i32 s16, s2, s16
	s_mul_i32 s2, s16, 0xffff9700
	s_add_i32 s20, s30, s2
	s_cmpk_gt_i32 s20, 0x6ff
	s_mov_b64 s[18:19], -1
	s_cbranch_scc0 .LBB0_28
	s_cmpk_gt_u32 s20, 0x7ff
	s_cbranch_scc0 .LBB0_25
	s_cmpk_gt_u32 s20, 0x8ff
	s_cbranch_scc0 .LBB0_22
	s_cmpk_gt_u32 s20, 0x48ff
	s_cbranch_scc0 .LBB0_19
	s_lshl_b32 s19, s30, 1
	s_add_i32 s2, s20, 0xffffb700
	s_and_b32 s18, s45, 0x3c0
	s_and_b32 s19, s19, 32
	s_lshr_b32 s2, s2, 8
	s_or_b32 s21, s19, s18
	s_lshl_b32 s18, s16, 5
	s_lshl_b32 s17, s30, 2
	s_add_i32 s18, s2, s18
	s_and_b32 s17, s17, 0x380
	s_ashr_i32 s19, s18, 31
	s_lshl_b64 s[22:23], s[18:19], 22
	s_lshl_b32 s2, s17, 12
	s_waitcnt lgkmcnt(0)
	s_add_u32 s22, s6, s22
	s_addc_u32 s23, s7, s23
	s_add_u32 s2, s22, s2
	s_addc_u32 s23, s23, 0
	s_lshl_b32 s22, s21, 2
	s_add_u32 s22, s2, s22
	s_addc_u32 s23, s23, 0
	v_lshl_add_u64 v[2:3], s[22:23], 0, v[106:107]
	v_lshlrev_b32_e32 v66, 2, v184
	v_lshl_add_u64 v[62:63], v[2:3], 0, v[66:67]
	v_add_co_u32_e32 v6, vcc, s48, v62
	s_lshl_b64 s[18:19], s[18:19], 20
	s_nop 0
	v_addc_co_u32_e32 v7, vcc, 0, v63, vcc
	v_add_co_u32_e32 v10, vcc, s49, v62
	global_load_dwordx4 v[2:5], v[62:63], off nt
	s_nop 0
	global_load_dwordx4 v[6:9], v[6:7], off nt
	v_addc_co_u32_e32 v11, vcc, 0, v63, vcc
	v_add_co_u32_e32 v14, vcc, s50, v62
	s_add_u32 s2, s31, s18
	s_nop 0
	v_addc_co_u32_e32 v15, vcc, 0, v63, vcc
	global_load_dwordx4 v[10:13], v[10:11], off nt
	s_nop 0
	global_load_dwordx4 v[14:17], v[14:15], off nt
	v_add_co_u32_e32 v18, vcc, s51, v62
	s_addc_u32 s18, s33, s19
	s_nop 0
	v_addc_co_u32_e32 v19, vcc, 0, v63, vcc
	v_add_co_u32_e32 v22, vcc, s52, v62
	s_lshl_b32 s19, s21, 10
	s_nop 0
	v_addc_co_u32_e32 v23, vcc, 0, v63, vcc
	global_load_dwordx4 v[18:21], v[18:19], off nt
	s_nop 0
	global_load_dwordx4 v[22:25], v[22:23], off nt
	v_add_co_u32_e32 v26, vcc, s53, v62
	s_add_u32 s2, s2, s19
	s_nop 0
	v_addc_co_u32_e32 v27, vcc, 0, v63, vcc
	v_add_co_u32_e32 v30, vcc, s54, v62
	s_addc_u32 s19, s18, 0
	s_nop 0
	v_addc_co_u32_e32 v31, vcc, 0, v63, vcc
	global_load_dwordx4 v[26:29], v[26:27], off nt
	s_nop 0
	global_load_dwordx4 v[30:33], v[30:31], off nt
	v_add_co_u32_e32 v34, vcc, s55, v62
	s_add_u32 s18, s2, s17
	s_nop 0
	v_addc_co_u32_e32 v35, vcc, 0, v63, vcc
	v_add_co_u32_e32 v38, vcc, s56, v62
	s_addc_u32 s19, s19, 0
	s_nop 0
	v_addc_co_u32_e32 v39, vcc, 0, v63, vcc
	global_load_dwordx4 v[34:37], v[34:35], off nt
	s_nop 0
	global_load_dwordx4 v[38:41], v[38:39], off nt
	v_add_co_u32_e32 v42, vcc, s57, v62
	s_nop 1
	v_addc_co_u32_e32 v43, vcc, 0, v63, vcc
	v_add_co_u32_e32 v46, vcc, s58, v62
	s_nop 1
	v_addc_co_u32_e32 v47, vcc, 0, v63, vcc
	global_load_dwordx4 v[42:45], v[42:43], off nt
	s_nop 0
	global_load_dwordx4 v[46:49], v[46:47], off nt
	v_add_co_u32_e32 v50, vcc, s59, v62
	s_nop 1
	v_addc_co_u32_e32 v51, vcc, 0, v63, vcc
	global_load_dwordx4 v[50:53], v[50:51], off nt
	v_add_co_u32_e32 v54, vcc, s60, v62
	s_nop 1
	v_addc_co_u32_e32 v55, vcc, 0, v63, vcc
	global_load_dwordx4 v[54:57], v[54:55], off nt
	v_add_co_u32_e32 v58, vcc, s61, v62
	s_nop 1
	v_addc_co_u32_e32 v59, vcc, 0, v63, vcc
	global_load_dwordx4 v[58:61], v[58:59], off nt
	v_add_co_u32_e32 v62, vcc, s62, v62
	s_nop 1
	v_addc_co_u32_e32 v63, vcc, 0, v63, vcc
	global_load_dwordx4 v[62:65], v[62:63], off nt
	s_waitcnt vmcnt(15)
	ds_write2_b32 v71, v2, v3 offset1:1
	ds_write2_b32 v71, v4, v5 offset0:2 offset1:3
	v_add_u32_e32 v2, 0x420, v71
	s_waitcnt vmcnt(14)
	ds_write2_b32 v2, v6, v7 offset1:1
	v_add_u32_e32 v2, 0x428, v71
	ds_write2_b32 v2, v8, v9 offset1:1
	v_add_u32_e32 v2, 0x840, v71
	s_waitcnt vmcnt(13)
	ds_write2_b32 v2, v10, v11 offset1:1
	v_add_u32_e32 v2, 0x848, v71
	ds_write2_b32 v2, v12, v13 offset1:1
	v_add_u32_e32 v2, 0xc60, v71
	s_waitcnt vmcnt(12)
	ds_write2_b32 v2, v14, v15 offset1:1
	v_add_u32_e32 v2, 0xc68, v71
	ds_write2_b32 v2, v16, v17 offset1:1
	v_add_u32_e32 v2, 0x1080, v71
	s_waitcnt vmcnt(11)
	ds_write2_b32 v2, v18, v19 offset1:1
	v_add_u32_e32 v2, 0x1088, v71
	ds_write2_b32 v2, v20, v21 offset1:1
	v_add_u32_e32 v2, 0x14a0, v71
	s_waitcnt vmcnt(10)
	ds_write2_b32 v2, v22, v23 offset1:1
	v_add_u32_e32 v2, 0x14a8, v71
	ds_write2_b32 v2, v24, v25 offset1:1
	v_add_u32_e32 v2, 0x18c0, v71
	s_waitcnt vmcnt(9)
	ds_write2_b32 v2, v26, v27 offset1:1
	v_add_u32_e32 v2, 0x18c8, v71
	ds_write2_b32 v2, v28, v29 offset1:1
	v_add_u32_e32 v2, 0x1ce0, v71
	s_waitcnt vmcnt(8)
	ds_write2_b32 v2, v30, v31 offset1:1
	v_add_u32_e32 v2, 0x1ce8, v71
	ds_write2_b32 v2, v32, v33 offset1:1
	v_add_u32_e32 v2, 0x2100, v71
	s_waitcnt vmcnt(7)
	ds_write2_b32 v2, v34, v35 offset1:1
	v_add_u32_e32 v2, 0x2108, v71
	ds_write2_b32 v2, v36, v37 offset1:1
	v_add_u32_e32 v2, 0x2520, v71
	s_waitcnt vmcnt(6)
	ds_write2_b32 v2, v38, v39 offset1:1
	v_add_u32_e32 v2, 0x2528, v71
	ds_write2_b32 v2, v40, v41 offset1:1
	v_add_u32_e32 v2, 0x2940, v71
	v_lshl_add_u64 v[38:39], s[18:19], 0, v[68:69]
	v_lshl_add_u64 v[40:41], v[38:39], 0, v[108:109]
	s_mov_b64 s[18:19], 0
	s_waitcnt vmcnt(5)
	ds_write2_b32 v2, v42, v43 offset1:1
	v_add_u32_e32 v2, 0x2948, v71
	ds_write2_b32 v2, v44, v45 offset1:1
	v_add_u32_e32 v2, 0x2d60, v71
	s_waitcnt vmcnt(4)
	ds_write2_b32 v2, v46, v47 offset1:1
	v_add_u32_e32 v2, 0x2d68, v71
	ds_write2_b32 v2, v48, v49 offset1:1
	v_add_u32_e32 v2, 0x3180, v71
	s_waitcnt vmcnt(3)
	ds_write2_b32 v2, v50, v51 offset1:1
	v_add_u32_e32 v2, 0x3188, v71
	ds_write2_b32 v2, v52, v53 offset1:1
	v_add_u32_e32 v2, 0x35a0, v71
	v_add_u32_e32 v42, 0x400, v119
	s_waitcnt vmcnt(2)
	ds_write2_b32 v2, v54, v55 offset1:1
	v_add_u32_e32 v2, 0x35a8, v71
	ds_write2_b32 v2, v56, v57 offset1:1
	v_add_u32_e32 v2, 0x39c0, v71
	s_waitcnt vmcnt(1)
	ds_write2_b32 v2, v58, v59 offset1:1
	v_add_u32_e32 v2, 0x39c8, v71
	ds_write2_b32 v2, v60, v61 offset1:1
	v_add_u32_e32 v2, 0x3de0, v71
	s_waitcnt vmcnt(0)
	ds_write2_b32 v2, v62, v63 offset1:1
	v_add_u32_e32 v2, 0x3de8, v71
	ds_write2_b32 v2, v64, v65 offset1:1
	s_waitcnt lgkmcnt(0)
	ds_read2_b32 v[6:7], v119 offset0:66 offset1:74
	ds_read2_b32 v[8:9], v119 offset0:99 offset1:107
	ds_read2_b32 v[10:11], v119 offset1:8
	ds_read2_b32 v[12:13], v119 offset0:33 offset1:41
	v_mov_b32_e32 v2, v67
	s_waitcnt lgkmcnt(3)
	v_mul_f32_e32 v3, 0x42000000, v6
	ds_read2_b32 v[14:15], v119 offset0:198 offset1:206
	ds_read2_b32 v[16:17], v119 offset0:231 offset1:239
	ds_read2_b32 v[18:19], v119 offset0:132 offset1:140
	ds_read2_b32 v[20:21], v119 offset0:165 offset1:173
	s_waitcnt lgkmcnt(5)
	v_mul_f32_e32 v5, 0x42000000, v10
	s_waitcnt lgkmcnt(4)
	v_mul_f32_e32 v6, 0x42000000, v12
	v_cvt_pk_fp8_f32 v2, v5, v6
	v_mul_f32_e32 v4, 0x42000000, v8
	s_waitcnt lgkmcnt(1)
	v_mul_f32_e32 v6, 0x42000000, v18
	s_waitcnt lgkmcnt(0)
	v_mul_f32_e32 v8, 0x42000000, v20
	v_cvt_pk_fp8_f32 v2, v3, v4 op_sel:[0,0,1]
	v_mov_b32_e32 v3, v67
	ds_read2_b32 v[22:23], v42 offset0:74 offset1:82
	ds_read2_b32 v[24:25], v42 offset0:107 offset1:115
	ds_read2_b32 v[26:27], v42 offset0:8 offset1:16
	ds_read2_b32 v[28:29], v42 offset0:41 offset1:49
	v_cvt_pk_fp8_f32 v3, v6, v8
	ds_read2_b32 v[30:31], v42 offset0:140 offset1:148
	ds_read2_b32 v[32:33], v42 offset0:173 offset1:181
	v_mul_f32_e32 v4, 0x42000000, v14
	v_mul_f32_e32 v5, 0x42000000, v16
	v_cvt_pk_fp8_f32 v3, v4, v5 op_sel:[0,0,1]
	s_waitcnt lgkmcnt(3)
	v_mul_f32_e32 v5, 0x42000000, v26
	s_waitcnt lgkmcnt(2)
	v_mul_f32_e32 v10, 0x42000000, v28
	v_mov_b32_e32 v4, v67
	ds_read2_b32 v[34:35], v42 offset0:206 offset1:214
	ds_read2_b32 v[36:37], v42 offset0:239 offset1:247
	v_cvt_pk_fp8_f32 v4, v5, v10
	s_waitcnt lgkmcnt(3)
	v_mul_f32_e32 v10, 0x42000000, v30
	s_waitcnt lgkmcnt(2)
	v_mul_f32_e32 v12, 0x42000000, v32
	v_mov_b32_e32 v5, v67
	v_cvt_pk_fp8_f32 v5, v10, v12
	v_mul_f32_e32 v6, 0x42000000, v22
	v_mul_f32_e32 v8, 0x42000000, v24
	v_cvt_pk_fp8_f32 v4, v6, v8 op_sel:[0,0,1]
	s_waitcnt lgkmcnt(1)
	v_mul_f32_e32 v6, 0x42000000, v34
	s_waitcnt lgkmcnt(0)
	v_mul_f32_e32 v8, 0x42000000, v36
	v_cvt_pk_fp8_f32 v5, v6, v8 op_sel:[0,0,1]
	v_mul_f32_e32 v6, 0x42000000, v13
	v_mul_f32_e32 v8, 0x42000000, v29
	global_store_dwordx4 v[40:41], v[2:5], off nt
	s_nop 1
	v_mul_f32_e32 v3, 0x42000000, v11
	v_mov_b32_e32 v2, v67
	v_mul_f32_e32 v4, 0x42000000, v7
	v_cvt_pk_fp8_f32 v2, v3, v6
	v_mul_f32_e32 v6, 0x42000000, v19
	v_mul_f32_e32 v7, 0x42000000, v21
	v_mov_b32_e32 v3, v67
	v_cvt_pk_fp8_f32 v3, v6, v7
	v_mul_f32_e32 v5, 0x42000000, v9
	v_cvt_pk_fp8_f32 v2, v4, v5 op_sel:[0,0,1]
	v_mul_f32_e32 v4, 0x42000000, v15
	v_mul_f32_e32 v5, 0x42000000, v17
	v_cvt_pk_fp8_f32 v3, v4, v5 op_sel:[0,0,1]
	v_mul_f32_e32 v5, 0x42000000, v27
	v_mov_b32_e32 v4, v67
	v_cvt_pk_fp8_f32 v4, v5, v8
	v_mul_f32_e32 v8, 0x42000000, v31
	v_mul_f32_e32 v9, 0x42000000, v33
	v_mov_b32_e32 v5, v67
	v_cvt_pk_fp8_f32 v5, v8, v9
	v_mul_f32_e32 v6, 0x42000000, v23
	v_mul_f32_e32 v7, 0x42000000, v25
	v_cvt_pk_fp8_f32 v4, v6, v7 op_sel:[0,0,1]
	v_mul_f32_e32 v6, 0x42000000, v35
	v_mul_f32_e32 v7, 0x42000000, v37
	ds_read2_b32 v[8:9], v119 offset0:82 offset1:90
	ds_read2_b32 v[10:11], v119 offset0:115 offset1:123
	ds_read2_b32 v[12:13], v119 offset0:16 offset1:24
	ds_read2_b32 v[14:15], v119 offset0:49 offset1:57
	v_cvt_pk_fp8_f32 v5, v6, v7 op_sel:[0,0,1]
	v_lshl_add_u64 v[6:7], v[38:39], 0, v[72:73]
	global_store_dwordx4 v[6:7], v[2:5], off nt
	s_waitcnt lgkmcnt(1)
	s_nop 0
	v_mul_f32_e32 v5, 0x42000000, v12
	s_waitcnt lgkmcnt(0)
	v_mul_f32_e32 v6, 0x42000000, v14
	v_mov_b32_e32 v2, v67
	v_cvt_pk_fp8_f32 v2, v5, v6
	ds_read2_b32 v[16:17], v119 offset0:214 offset1:222
	ds_read2_b32 v[18:19], v119 offset0:247 offset1:255
	ds_read2_b32 v[6:7], v119 offset0:148 offset1:156
	ds_read2_b32 v[20:21], v119 offset0:181 offset1:189
	v_mul_f32_e32 v3, 0x42000000, v8
	v_mul_f32_e32 v4, 0x42000000, v10
	v_cvt_pk_fp8_f32 v2, v3, v4 op_sel:[0,0,1]
	s_waitcnt lgkmcnt(1)
	v_mul_f32_e32 v6, 0x42000000, v6
	s_waitcnt lgkmcnt(0)
	v_mul_f32_e32 v8, 0x42000000, v20
	v_mov_b32_e32 v3, v67
	ds_read2_b32 v[22:23], v42 offset0:90 offset1:98
	ds_read2_b32 v[24:25], v42 offset0:123 offset1:131
	ds_read2_b32 v[26:27], v42 offset0:24 offset1:32
	ds_read2_b32 v[28:29], v42 offset0:57 offset1:65
	v_cvt_pk_fp8_f32 v3, v6, v8
	v_mul_f32_e32 v4, 0x42000000, v16
	v_mul_f32_e32 v5, 0x42000000, v18
	ds_read2_b32 v[30:31], v42 offset0:156 offset1:164
	ds_read2_b32 v[32:33], v42 offset0:189 offset1:197
	ds_read2_b32 v[34:35], v42 offset0:222 offset1:230
	v_cvt_pk_fp8_f32 v3, v4, v5 op_sel:[0,0,1]
	s_waitcnt lgkmcnt(4)
	v_mul_f32_e32 v5, 0x42000000, v26
	s_waitcnt lgkmcnt(3)
	v_mul_f32_e32 v10, 0x42000000, v28
	v_mov_b32_e32 v4, v67
	v_cvt_pk_fp8_f32 v4, v5, v10
	v_add_u32_e32 v5, 0x600, v119
	ds_read2_b32 v[36:37], v5 offset0:127 offset1:135
	s_waitcnt lgkmcnt(3)
	v_mul_f32_e32 v10, 0x42000000, v30
	s_waitcnt lgkmcnt(2)
	v_mul_f32_e32 v12, 0x42000000, v32
	v_mov_b32_e32 v5, v67
	v_cvt_pk_fp8_f32 v5, v10, v12
	v_mul_f32_e32 v6, 0x42000000, v22
	v_mul_f32_e32 v8, 0x42000000, v24
	v_cvt_pk_fp8_f32 v4, v6, v8 op_sel:[0,0,1]
	s_waitcnt lgkmcnt(1)
	v_mul_f32_e32 v6, 0x42000000, v34
	s_waitcnt lgkmcnt(0)
	v_mul_f32_e32 v8, 0x42000000, v36
	v_cvt_pk_fp8_f32 v5, v6, v8 op_sel:[0,0,1]
	v_mul_f32_e32 v8, 0x42000000, v9
	v_mul_f32_e32 v9, 0x42000000, v11
	v_mul_f32_e32 v10, 0x42000000, v13
	v_mul_f32_e32 v11, 0x42000000, v15
	v_mov_b32_e32 v6, v67
	v_cvt_pk_fp8_f32 v6, v10, v11
	v_mul_f32_e32 v10, 0x42000000, v7
	v_mul_f32_e32 v11, 0x42000000, v21
	v_mov_b32_e32 v7, v67
	v_cvt_pk_fp8_f32 v7, v10, v11
	v_cvt_pk_fp8_f32 v6, v8, v9 op_sel:[0,0,1]
	v_mul_f32_e32 v8, 0x42000000, v17
	v_mul_f32_e32 v9, 0x42000000, v19
	v_cvt_pk_fp8_f32 v7, v8, v9 op_sel:[0,0,1]
	v_mul_f32_e32 v9, 0x42000000, v27
	v_mul_f32_e32 v12, 0x42000000, v29
	v_mov_b32_e32 v8, v67
	v_cvt_pk_fp8_f32 v8, v9, v12
	v_mul_f32_e32 v12, 0x42000000, v31
	v_mul_f32_e32 v13, 0x42000000, v33
	v_mov_b32_e32 v9, v67
	v_cvt_pk_fp8_f32 v9, v12, v13
	v_mul_f32_e32 v10, 0x42000000, v23
	v_mul_f32_e32 v11, 0x42000000, v25
	v_cvt_pk_fp8_f32 v8, v10, v11 op_sel:[0,0,1]
	v_mul_f32_e32 v10, 0x42000000, v35
	v_mul_f32_e32 v11, 0x42000000, v37
	v_cvt_pk_fp8_f32 v9, v10, v11 op_sel:[0,0,1]
	v_lshl_add_u64 v[10:11], v[38:39], 0, v[78:79]
	global_store_dwordx4 v[10:11], v[2:5], off nt
	s_nop 1
	v_lshl_add_u64 v[2:3], v[38:39], 0, v[84:85]
	global_store_dwordx4 v[2:3], v[6:9], off nt
	s_waitcnt lgkmcnt(0)
.LBB0_19:
	s_andn2_b64 vcc, exec, s[18:19]
	s_cbranch_vccnz .LBB0_21
	s_and_b32 s18, s45, 0x7c0
	s_and_b32 s19, s30, 32
	s_add_i32 s2, s20, 0xfffff700
	s_or_b32 s21, s18, s19
	s_lshr_b32 s19, s45, 1
	s_lshr_b32 s17, s2, 9
	s_lshl_b32 s2, s16, 9
	s_and_b32 s18, s21, 0xe0
	s_and_b32 s19, s19, 0x380
	s_sub_i32 s2, s47, s2
	s_or_b32 s22, s18, s19
	s_add_i32 s19, s19, s18
	s_and_b32 s2, s2, 0x380
	s_addk_i32 s19, 0x380
	s_cmpk_lt_u32 s18, 0x80
	s_cselect_b32 s24, s22, s19
	s_lshl_b32 s18, s16, 5
	s_add_i32 s18, s17, s18
	s_ashr_i32 s19, s18, 31
	s_lshl_b64 s[22:23], s[18:19], 23
	s_waitcnt lgkmcnt(0)
	s_add_u32 s17, s12, s22
	s_addc_u32 s22, s13, s23
	s_lshl_b32 s23, s2, 13
	s_add_u32 s17, s17, s23
	s_addc_u32 s23, s22, 0
	s_lshl_b32 s22, s24, 2
	s_add_u32 s22, s17, s22
	s_addc_u32 s23, s23, 0
	v_lshl_add_u64 v[2:3], s[22:23], 0, v[110:111]
	v_lshlrev_b32_e32 v66, 2, v184
	v_lshl_add_u64 v[62:63], v[2:3], 0, v[66:67]
	v_add_co_u32_e32 v6, vcc, s49, v62
	s_lshl_b64 s[18:19], s[18:19], 21
	s_nop 0
	v_addc_co_u32_e32 v7, vcc, 0, v63, vcc
	v_add_co_u32_e32 v10, vcc, s51, v62
	global_load_dwordx4 v[2:5], v[62:63], off nt
	s_nop 0
	global_load_dwordx4 v[6:9], v[6:7], off nt
	v_addc_co_u32_e32 v11, vcc, 0, v63, vcc
	v_add_co_u32_e32 v14, vcc, s53, v62
	s_add_u32 s17, s34, s18
	s_nop 0
	v_addc_co_u32_e32 v15, vcc, 0, v63, vcc
	global_load_dwordx4 v[10:13], v[10:11], off nt
	s_nop 0
	global_load_dwordx4 v[14:17], v[14:15], off nt
	v_add_co_u32_e32 v18, vcc, s55, v62
	s_addc_u32 s18, s35, s19
	s_nop 0
	v_addc_co_u32_e32 v19, vcc, 0, v63, vcc
	v_add_co_u32_e32 v22, vcc, s57, v62
	s_lshl_b32 s19, s21, 10
	s_nop 0
	v_addc_co_u32_e32 v23, vcc, 0, v63, vcc
	global_load_dwordx4 v[18:21], v[18:19], off nt
	s_nop 0
	global_load_dwordx4 v[22:25], v[22:23], off nt
	v_add_co_u32_e32 v26, vcc, s59, v62
	s_add_u32 s17, s17, s19
	s_nop 0
	v_addc_co_u32_e32 v27, vcc, 0, v63, vcc
	v_add_co_u32_e32 v30, vcc, s61, v62
	s_addc_u32 s19, s18, 0
	s_nop 0
	v_addc_co_u32_e32 v31, vcc, 0, v63, vcc
	global_load_dwordx4 v[26:29], v[26:27], off nt
	s_nop 0
	global_load_dwordx4 v[30:33], v[30:31], off nt
	v_add_co_u32_e32 v34, vcc, s63, v62
	s_add_u32 s18, s17, s2
	s_nop 0
	v_addc_co_u32_e32 v35, vcc, 0, v63, vcc
	v_add_co_u32_e32 v38, vcc, s64, v62
	s_addc_u32 s19, s19, 0
	s_nop 0
	v_addc_co_u32_e32 v39, vcc, 0, v63, vcc
	global_load_dwordx4 v[34:37], v[34:35], off nt
	s_nop 0
	global_load_dwordx4 v[38:41], v[38:39], off nt
	v_add_co_u32_e32 v42, vcc, s65, v62
	s_nop 1
	v_addc_co_u32_e32 v43, vcc, 0, v63, vcc
	v_add_co_u32_e32 v46, vcc, s66, v62
	s_nop 1
	v_addc_co_u32_e32 v47, vcc, 0, v63, vcc
	global_load_dwordx4 v[42:45], v[42:43], off nt
	s_nop 0
	global_load_dwordx4 v[46:49], v[46:47], off nt
	v_add_co_u32_e32 v50, vcc, s67, v62
	s_nop 1
	v_addc_co_u32_e32 v51, vcc, 0, v63, vcc
	global_load_dwordx4 v[50:53], v[50:51], off nt
	v_add_co_u32_e32 v54, vcc, s68, v62
	s_nop 1
	v_addc_co_u32_e32 v55, vcc, 0, v63, vcc
	global_load_dwordx4 v[54:57], v[54:55], off nt
	v_add_co_u32_e32 v58, vcc, s69, v62
	s_nop 1
	v_addc_co_u32_e32 v59, vcc, 0, v63, vcc
	global_load_dwordx4 v[58:61], v[58:59], off nt
	v_add_co_u32_e32 v62, vcc, s70, v62
	s_nop 1
	v_addc_co_u32_e32 v63, vcc, 0, v63, vcc
	global_load_dwordx4 v[62:65], v[62:63], off nt
	s_waitcnt vmcnt(15)
	ds_write2_b32 v71, v2, v3 offset1:1
	ds_write2_b32 v71, v4, v5 offset0:2 offset1:3
	v_add_u32_e32 v2, 0x420, v71
	s_waitcnt vmcnt(14)
	ds_write2_b32 v2, v6, v7 offset1:1
	v_add_u32_e32 v2, 0x428, v71
	ds_write2_b32 v2, v8, v9 offset1:1
	v_add_u32_e32 v2, 0x840, v71
	s_waitcnt vmcnt(13)
	ds_write2_b32 v2, v10, v11 offset1:1
	v_add_u32_e32 v2, 0x848, v71
	ds_write2_b32 v2, v12, v13 offset1:1
	v_add_u32_e32 v2, 0xc60, v71
	s_waitcnt vmcnt(12)
	ds_write2_b32 v2, v14, v15 offset1:1
	v_add_u32_e32 v2, 0xc68, v71
	ds_write2_b32 v2, v16, v17 offset1:1
	v_add_u32_e32 v2, 0x1080, v71
	s_waitcnt vmcnt(11)
	ds_write2_b32 v2, v18, v19 offset1:1
	v_add_u32_e32 v2, 0x1088, v71
	ds_write2_b32 v2, v20, v21 offset1:1
	v_add_u32_e32 v2, 0x14a0, v71
	s_waitcnt vmcnt(10)
	ds_write2_b32 v2, v22, v23 offset1:1
	v_add_u32_e32 v2, 0x14a8, v71
	ds_write2_b32 v2, v24, v25 offset1:1
	v_add_u32_e32 v2, 0x18c0, v71
	s_waitcnt vmcnt(9)
	ds_write2_b32 v2, v26, v27 offset1:1
	v_add_u32_e32 v2, 0x18c8, v71
	ds_write2_b32 v2, v28, v29 offset1:1
	v_add_u32_e32 v2, 0x1ce0, v71
	s_waitcnt vmcnt(8)
	ds_write2_b32 v2, v30, v31 offset1:1
	v_add_u32_e32 v2, 0x1ce8, v71
	ds_write2_b32 v2, v32, v33 offset1:1
	v_add_u32_e32 v2, 0x2100, v71
	s_waitcnt vmcnt(7)
	ds_write2_b32 v2, v34, v35 offset1:1
	v_add_u32_e32 v2, 0x2108, v71
	ds_write2_b32 v2, v36, v37 offset1:1
	v_add_u32_e32 v2, 0x2520, v71
	s_waitcnt vmcnt(6)
	ds_write2_b32 v2, v38, v39 offset1:1
	v_add_u32_e32 v2, 0x2528, v71
	ds_write2_b32 v2, v40, v41 offset1:1
	v_add_u32_e32 v2, 0x2940, v71
	v_lshl_add_u64 v[38:39], s[18:19], 0, v[68:69]
	v_lshl_add_u64 v[40:41], v[38:39], 0, v[108:109]
	s_waitcnt vmcnt(5)
	ds_write2_b32 v2, v42, v43 offset1:1
	v_add_u32_e32 v2, 0x2948, v71
	ds_write2_b32 v2, v44, v45 offset1:1
	v_add_u32_e32 v2, 0x2d60, v71
	s_waitcnt vmcnt(4)
	ds_write2_b32 v2, v46, v47 offset1:1
	v_add_u32_e32 v2, 0x2d68, v71
	ds_write2_b32 v2, v48, v49 offset1:1
	v_add_u32_e32 v2, 0x3180, v71
	s_waitcnt vmcnt(3)
	ds_write2_b32 v2, v50, v51 offset1:1
	v_add_u32_e32 v2, 0x3188, v71
	ds_write2_b32 v2, v52, v53 offset1:1
	v_add_u32_e32 v2, 0x35a0, v71
	v_add_u32_e32 v42, 0x400, v119
	s_waitcnt vmcnt(2)
	ds_write2_b32 v2, v54, v55 offset1:1
	v_add_u32_e32 v2, 0x35a8, v71
	ds_write2_b32 v2, v56, v57 offset1:1
	v_add_u32_e32 v2, 0x39c0, v71
	s_waitcnt vmcnt(1)
	ds_write2_b32 v2, v58, v59 offset1:1
	v_add_u32_e32 v2, 0x39c8, v71
	ds_write2_b32 v2, v60, v61 offset1:1
	v_add_u32_e32 v2, 0x3de0, v71
	s_waitcnt vmcnt(0)
	ds_write2_b32 v2, v62, v63 offset1:1
	v_add_u32_e32 v2, 0x3de8, v71
	ds_write2_b32 v2, v64, v65 offset1:1
	s_waitcnt lgkmcnt(0)
	ds_read2_b32 v[6:7], v119 offset0:66 offset1:74
	ds_read2_b32 v[8:9], v119 offset0:99 offset1:107
	ds_read2_b32 v[10:11], v119 offset1:8
	ds_read2_b32 v[12:13], v119 offset0:33 offset1:41
	v_mov_b32_e32 v2, v67
	s_waitcnt lgkmcnt(3)
	v_mul_f32_e32 v3, 0x42000000, v6
	ds_read2_b32 v[14:15], v119 offset0:198 offset1:206
	ds_read2_b32 v[16:17], v119 offset0:231 offset1:239
	ds_read2_b32 v[18:19], v119 offset0:132 offset1:140
	ds_read2_b32 v[20:21], v119 offset0:165 offset1:173
	s_waitcnt lgkmcnt(5)
	v_mul_f32_e32 v5, 0x42000000, v10
	s_waitcnt lgkmcnt(4)
	v_mul_f32_e32 v6, 0x42000000, v12
	v_cvt_pk_fp8_f32 v2, v5, v6
	v_mul_f32_e32 v4, 0x42000000, v8
	s_waitcnt lgkmcnt(1)
	v_mul_f32_e32 v6, 0x42000000, v18
	s_waitcnt lgkmcnt(0)
	v_mul_f32_e32 v8, 0x42000000, v20
	v_cvt_pk_fp8_f32 v2, v3, v4 op_sel:[0,0,1]
	v_mov_b32_e32 v3, v67
	ds_read2_b32 v[22:23], v42 offset0:74 offset1:82
	ds_read2_b32 v[24:25], v42 offset0:107 offset1:115
	ds_read2_b32 v[26:27], v42 offset0:8 offset1:16
	ds_read2_b32 v[28:29], v42 offset0:41 offset1:49
	v_cvt_pk_fp8_f32 v3, v6, v8
	ds_read2_b32 v[30:31], v42 offset0:140 offset1:148
	ds_read2_b32 v[32:33], v42 offset0:173 offset1:181
	v_mul_f32_e32 v4, 0x42000000, v14
	v_mul_f32_e32 v5, 0x42000000, v16
	v_cvt_pk_fp8_f32 v3, v4, v5 op_sel:[0,0,1]
	s_waitcnt lgkmcnt(3)
	v_mul_f32_e32 v5, 0x42000000, v26
	s_waitcnt lgkmcnt(2)
	v_mul_f32_e32 v10, 0x42000000, v28
	v_mov_b32_e32 v4, v67
	ds_read2_b32 v[34:35], v42 offset0:206 offset1:214
	ds_read2_b32 v[36:37], v42 offset0:239 offset1:247
	v_cvt_pk_fp8_f32 v4, v5, v10
	s_waitcnt lgkmcnt(3)
	v_mul_f32_e32 v10, 0x42000000, v30
	s_waitcnt lgkmcnt(2)
	v_mul_f32_e32 v12, 0x42000000, v32
	v_mov_b32_e32 v5, v67
	v_cvt_pk_fp8_f32 v5, v10, v12
	v_mul_f32_e32 v6, 0x42000000, v22
	v_mul_f32_e32 v8, 0x42000000, v24
	v_cvt_pk_fp8_f32 v4, v6, v8 op_sel:[0,0,1]
	s_waitcnt lgkmcnt(1)
	v_mul_f32_e32 v6, 0x42000000, v34
	s_waitcnt lgkmcnt(0)
	v_mul_f32_e32 v8, 0x42000000, v36
	v_cvt_pk_fp8_f32 v5, v6, v8 op_sel:[0,0,1]
	v_mul_f32_e32 v6, 0x42000000, v13
	v_mul_f32_e32 v8, 0x42000000, v29
	global_store_dwordx4 v[40:41], v[2:5], off nt
	s_nop 1
	v_mul_f32_e32 v3, 0x42000000, v11
	v_mov_b32_e32 v2, v67
	v_mul_f32_e32 v4, 0x42000000, v7
	v_cvt_pk_fp8_f32 v2, v3, v6
	v_mul_f32_e32 v6, 0x42000000, v19
	v_mul_f32_e32 v7, 0x42000000, v21
	v_mov_b32_e32 v3, v67
	v_cvt_pk_fp8_f32 v3, v6, v7
	v_mul_f32_e32 v5, 0x42000000, v9
	v_cvt_pk_fp8_f32 v2, v4, v5 op_sel:[0,0,1]
	v_mul_f32_e32 v4, 0x42000000, v15
	v_mul_f32_e32 v5, 0x42000000, v17
	v_cvt_pk_fp8_f32 v3, v4, v5 op_sel:[0,0,1]
	v_mul_f32_e32 v5, 0x42000000, v27
	v_mov_b32_e32 v4, v67
	v_cvt_pk_fp8_f32 v4, v5, v8
	v_mul_f32_e32 v8, 0x42000000, v31
	v_mul_f32_e32 v9, 0x42000000, v33
	v_mov_b32_e32 v5, v67
	v_cvt_pk_fp8_f32 v5, v8, v9
	v_mul_f32_e32 v6, 0x42000000, v23
	v_mul_f32_e32 v7, 0x42000000, v25
	v_cvt_pk_fp8_f32 v4, v6, v7 op_sel:[0,0,1]
	v_mul_f32_e32 v6, 0x42000000, v35
	v_mul_f32_e32 v7, 0x42000000, v37
	ds_read2_b32 v[8:9], v119 offset0:82 offset1:90
	ds_read2_b32 v[10:11], v119 offset0:115 offset1:123
	ds_read2_b32 v[12:13], v119 offset0:16 offset1:24
	ds_read2_b32 v[14:15], v119 offset0:49 offset1:57
	v_cvt_pk_fp8_f32 v5, v6, v7 op_sel:[0,0,1]
	v_lshl_add_u64 v[6:7], v[38:39], 0, v[72:73]
	global_store_dwordx4 v[6:7], v[2:5], off nt
	s_waitcnt lgkmcnt(1)
	s_nop 0
	v_mul_f32_e32 v5, 0x42000000, v12
	s_waitcnt lgkmcnt(0)
	v_mul_f32_e32 v6, 0x42000000, v14
	v_mov_b32_e32 v2, v67
	v_cvt_pk_fp8_f32 v2, v5, v6
	ds_read2_b32 v[16:17], v119 offset0:214 offset1:222
	ds_read2_b32 v[18:19], v119 offset0:247 offset1:255
	ds_read2_b32 v[6:7], v119 offset0:148 offset1:156
	ds_read2_b32 v[20:21], v119 offset0:181 offset1:189
	v_mul_f32_e32 v3, 0x42000000, v8
	v_mul_f32_e32 v4, 0x42000000, v10
	v_cvt_pk_fp8_f32 v2, v3, v4 op_sel:[0,0,1]
	s_waitcnt lgkmcnt(1)
	v_mul_f32_e32 v6, 0x42000000, v6
	s_waitcnt lgkmcnt(0)
	v_mul_f32_e32 v8, 0x42000000, v20
	v_mov_b32_e32 v3, v67
	ds_read2_b32 v[22:23], v42 offset0:90 offset1:98
	ds_read2_b32 v[24:25], v42 offset0:123 offset1:131
	ds_read2_b32 v[26:27], v42 offset0:24 offset1:32
	ds_read2_b32 v[28:29], v42 offset0:57 offset1:65
	v_cvt_pk_fp8_f32 v3, v6, v8
	v_mul_f32_e32 v4, 0x42000000, v16
	v_mul_f32_e32 v5, 0x42000000, v18
	ds_read2_b32 v[30:31], v42 offset0:156 offset1:164
	ds_read2_b32 v[32:33], v42 offset0:189 offset1:197
	ds_read2_b32 v[34:35], v42 offset0:222 offset1:230
	v_cvt_pk_fp8_f32 v3, v4, v5 op_sel:[0,0,1]
	s_waitcnt lgkmcnt(4)
	v_mul_f32_e32 v5, 0x42000000, v26
	s_waitcnt lgkmcnt(3)
	v_mul_f32_e32 v10, 0x42000000, v28
	v_mov_b32_e32 v4, v67
	v_cvt_pk_fp8_f32 v4, v5, v10
	v_add_u32_e32 v5, 0x600, v119
	ds_read2_b32 v[36:37], v5 offset0:127 offset1:135
	s_waitcnt lgkmcnt(3)
	v_mul_f32_e32 v10, 0x42000000, v30
	s_waitcnt lgkmcnt(2)
	v_mul_f32_e32 v12, 0x42000000, v32
	v_mov_b32_e32 v5, v67
	v_cvt_pk_fp8_f32 v5, v10, v12
	v_mul_f32_e32 v6, 0x42000000, v22
	v_mul_f32_e32 v8, 0x42000000, v24
	v_cvt_pk_fp8_f32 v4, v6, v8 op_sel:[0,0,1]
	s_waitcnt lgkmcnt(1)
	v_mul_f32_e32 v6, 0x42000000, v34
	s_waitcnt lgkmcnt(0)
	v_mul_f32_e32 v8, 0x42000000, v36
	v_cvt_pk_fp8_f32 v5, v6, v8 op_sel:[0,0,1]
	v_mul_f32_e32 v8, 0x42000000, v9
	v_mul_f32_e32 v9, 0x42000000, v11
	v_mul_f32_e32 v10, 0x42000000, v13
	v_mul_f32_e32 v11, 0x42000000, v15
	v_mov_b32_e32 v6, v67
	v_cvt_pk_fp8_f32 v6, v10, v11
	v_mul_f32_e32 v10, 0x42000000, v7
	v_mul_f32_e32 v11, 0x42000000, v21
	v_mov_b32_e32 v7, v67
	v_cvt_pk_fp8_f32 v7, v10, v11
	v_cvt_pk_fp8_f32 v6, v8, v9 op_sel:[0,0,1]
	v_mul_f32_e32 v8, 0x42000000, v17
	v_mul_f32_e32 v9, 0x42000000, v19
	v_cvt_pk_fp8_f32 v7, v8, v9 op_sel:[0,0,1]
	v_mul_f32_e32 v9, 0x42000000, v27
	v_mul_f32_e32 v12, 0x42000000, v29
	v_mov_b32_e32 v8, v67
	v_cvt_pk_fp8_f32 v8, v9, v12
	v_mul_f32_e32 v12, 0x42000000, v31
	v_mul_f32_e32 v13, 0x42000000, v33
	v_mov_b32_e32 v9, v67
	v_cvt_pk_fp8_f32 v9, v12, v13
	v_mul_f32_e32 v10, 0x42000000, v23
	v_mul_f32_e32 v11, 0x42000000, v25
	v_cvt_pk_fp8_f32 v8, v10, v11 op_sel:[0,0,1]
	v_mul_f32_e32 v10, 0x42000000, v35
	v_mul_f32_e32 v11, 0x42000000, v37
	v_cvt_pk_fp8_f32 v9, v10, v11 op_sel:[0,0,1]
	v_lshl_add_u64 v[10:11], v[38:39], 0, v[78:79]
	global_store_dwordx4 v[10:11], v[2:5], off nt
	s_nop 1
	v_lshl_add_u64 v[2:3], v[38:39], 0, v[84:85]
	global_store_dwordx4 v[2:3], v[6:9], off nt
	s_waitcnt lgkmcnt(0)

.LBB0_22:
	s_andn2_b64 vcc, exec, s[18:19]
	s_cbranch_vccnz .LBB0_24
	s_mul_i32 s2, s16, 0xfffe5c00
	s_add_i32 s2, s46, s2
	s_and_b32 s2, s2, 0x3fc0
	s_ashr_i32 s17, s16, 31
	s_addk_i32 s2, 0xe000
	s_lshl_b64 s[18:19], s[16:17], 22
	s_lshl_b64 s[22:23], s[2:3], 12
	s_waitcnt lgkmcnt(0)
	s_add_u32 s18, s10, s18
	s_addc_u32 s19, s11, s19
	s_add_u32 s18, s18, s22
	s_addc_u32 s19, s19, s23
	s_and_b32 s21, s45, 0x3c0
	s_lshl_b32 s22, s21, 2
	s_add_u32 s18, s18, s22
	s_addc_u32 s19, s19, 0
	v_lshlrev_b32_e32 v66, 2, v118
	v_lshl_add_u64 v[62:63], s[18:19], 0, v[66:67]
	v_lshl_add_u64 v[2:3], v[62:63], 0, v[120:121]
	global_load_dwordx4 v[2:5], v[2:3], off nt
	v_lshl_add_u64 v[34:35], v[62:63], 0, v[152:153]
	v_lshl_add_u64 v[38:39], v[62:63], 0, v[156:157]
	v_lshl_add_u64 v[6:7], v[62:63], 0, v[124:125]
	global_load_dwordx4 v[34:37], v[34:35], off nt
	v_lshl_add_u64 v[42:43], v[62:63], 0, v[160:161]
	global_load_dwordx4 v[38:41], v[38:39], off nt
	v_lshl_add_u64 v[10:11], v[62:63], 0, v[128:129]
	global_load_dwordx4 v[6:9], v[6:7], off nt
	v_lshl_add_u64 v[46:47], v[62:63], 0, v[164:165]
	global_load_dwordx4 v[42:45], v[42:43], off nt
	v_lshl_add_u64 v[14:15], v[62:63], 0, v[132:133]
	global_load_dwordx4 v[10:13], v[10:11], off nt
	v_lshl_add_u64 v[50:51], v[62:63], 0, v[168:169]
	global_load_dwordx4 v[46:49], v[46:47], off nt
	v_lshl_add_u64 v[18:19], v[62:63], 0, v[136:137]
	global_load_dwordx4 v[14:17], v[14:15], off nt
	v_lshl_add_u64 v[54:55], v[62:63], 0, v[172:173]
	global_load_dwordx4 v[50:53], v[50:51], off nt
	v_lshl_add_u64 v[22:23], v[62:63], 0, v[140:141]
	global_load_dwordx4 v[18:21], v[18:19], off nt
	v_lshl_add_u64 v[58:59], v[62:63], 0, v[176:177]
	global_load_dwordx4 v[54:57], v[54:55], off nt
	v_lshl_add_u64 v[26:27], v[62:63], 0, v[144:145]
	global_load_dwordx4 v[22:25], v[22:23], off nt
	v_lshl_add_u64 v[30:31], v[62:63], 0, v[148:149]
	global_load_dwordx4 v[58:61], v[58:59], off nt
	v_lshl_add_u64 v[62:63], v[62:63], 0, v[180:181]
	global_load_dwordx4 v[26:29], v[26:27], off nt
	v_add_u32_e32 v66, v189, v188
	global_load_dwordx4 v[62:65], v[62:63], off nt
	v_add_u32_e32 v186, 0x410, v66
	global_load_dwordx4 v[30:33], v[30:31], off nt
	v_add_u32_e32 v187, 0x418, v66
	v_add_u32_e32 v190, 0x820, v66
	v_add_u32_e32 v191, 0x828, v66
	v_add_u32_e32 v192, 0xc30, v66
	v_add_u32_e32 v193, 0xc38, v66
	v_add_u32_e32 v194, 0x1040, v66
	v_add_u32_e32 v195, 0x1048, v66
	v_add_u32_e32 v196, 0x1450, v66
	v_add_u32_e32 v197, 0x1458, v66
	v_add_u32_e32 v198, 0x1860, v66
	v_add_u32_e32 v199, 0x1868, v66
	v_add_u32_e32 v200, 0x1c70, v66
	v_add_u32_e32 v201, 0x1c78, v66
	v_add_u32_e32 v202, 0x2080, v66
	v_add_u32_e32 v203, 0x2088, v66
	v_add_u32_e32 v204, 0x2490, v66
	s_lshl_b64 s[18:19], s[16:17], 21
	s_add_u32 s17, s36, s18
	s_addc_u32 s18, s37, s19
	s_lshl_b32 s19, s21, 11
	s_add_u32 s17, s17, s19
	s_addc_u32 s21, s18, 0
	s_lshl_b64 s[18:19], s[2:3], 1
	s_add_u32 s18, s17, s18
	s_addc_u32 s19, s21, s19
	s_waitcnt vmcnt(15)
	ds_write2_b32 v66, v2, v3 offset1:1
	ds_write2_b32 v66, v4, v5 offset0:2 offset1:3
	s_waitcnt vmcnt(12)
	ds_write2_b32 v186, v6, v7 offset1:1
	ds_write2_b32 v187, v8, v9 offset1:1
	s_waitcnt vmcnt(10)
	ds_write2_b32 v190, v10, v11 offset1:1
	ds_write2_b32 v191, v12, v13 offset1:1
	s_waitcnt vmcnt(8)
	ds_write2_b32 v192, v14, v15 offset1:1
	ds_write2_b32 v193, v16, v17 offset1:1
	s_waitcnt vmcnt(6)
	ds_write2_b32 v194, v18, v19 offset1:1
	ds_write2_b32 v195, v20, v21 offset1:1
	s_waitcnt vmcnt(4)
	ds_write2_b32 v196, v22, v23 offset1:1
	ds_write2_b32 v197, v24, v25 offset1:1
	s_waitcnt vmcnt(2)
	ds_write2_b32 v198, v26, v27 offset1:1
	ds_write2_b32 v199, v28, v29 offset1:1
	s_waitcnt vmcnt(0)
	ds_write2_b32 v200, v30, v31 offset1:1
	ds_write2_b32 v201, v32, v33 offset1:1
	ds_write2_b32 v202, v34, v35 offset1:1
	ds_write2_b32 v203, v36, v37 offset1:1
	ds_write2_b32 v204, v38, v39 offset1:1
	v_add_u32_e32 v2, 0x2498, v66
	ds_write2_b32 v2, v40, v41 offset1:1
	v_add_u32_e32 v2, 0x28a0, v66
	ds_write2_b32 v2, v42, v43 offset1:1
	v_add_u32_e32 v2, 0x28a8, v66
	ds_write2_b32 v2, v44, v45 offset1:1
	v_add_u32_e32 v2, 0x2cb0, v66
	ds_write2_b32 v2, v46, v47 offset1:1
	v_add_u32_e32 v2, 0x2cb8, v66
	ds_write2_b32 v2, v48, v49 offset1:1
	v_add_u32_e32 v2, 0x30c0, v66
	ds_write2_b32 v2, v50, v51 offset1:1
	v_add_u32_e32 v2, 0x30c8, v66
	ds_write2_b32 v2, v52, v53 offset1:1
	v_add_u32_e32 v2, 0x34d0, v66
	ds_write2_b32 v2, v54, v55 offset1:1
	v_add_u32_e32 v2, 0x34d8, v66
	ds_write2_b32 v2, v56, v57 offset1:1
	v_add_u32_e32 v2, 0x38e0, v66
	ds_write2_b32 v2, v58, v59 offset1:1
	v_add_u32_e32 v2, 0x38e8, v66
	ds_write2_b32 v2, v60, v61 offset1:1
	v_add_u32_e32 v2, 0x3cf0, v66
	ds_write2_b32 v2, v62, v63 offset1:1
	v_add_u32_e32 v2, 0x3cf8, v66
	ds_write2_b32 v2, v64, v65 offset1:1
	s_waitcnt lgkmcnt(0)
	v_add_u32_e32 v26, 0x400, v185
	ds_read2_b32 v[6:7], v185 offset0:65 offset1:73
	ds_read2_b32 v[8:9], v185 offset1:8
	ds_read2_b32 v[10:11], v185 offset0:130 offset1:138
	ds_read2_b32 v[12:13], v185 offset0:195 offset1:203
	ds_read2_b32 v[14:15], v26 offset0:4 offset1:12
	ds_read2_b32 v[16:17], v26 offset0:69 offset1:77
	ds_read2_b32 v[18:19], v26 offset0:134 offset1:142
	ds_read2_b32 v[20:21], v26 offset0:199 offset1:207
	v_lshlrev_b32_e32 v66, 1, v70
	v_lshl_add_u64 v[22:23], s[18:19], 0, v[66:67]
	s_waitcnt lgkmcnt(6)
	v_cvt_pk_bf16_f32 v2, v8, v6
	s_waitcnt lgkmcnt(4)
	v_cvt_pk_bf16_f32 v3, v10, v12
	s_waitcnt lgkmcnt(2)
	v_cvt_pk_bf16_f32 v4, v14, v16
	s_waitcnt lgkmcnt(0)
	v_cvt_pk_bf16_f32 v5, v18, v20
	v_lshl_add_u64 v[24:25], v[22:23], 0, v[112:113]
	global_store_dwordx4 v[24:25], v[2:5], off nt
	s_nop 1
	v_cvt_pk_bf16_f32 v2, v9, v7
	v_cvt_pk_bf16_f32 v3, v11, v13
	v_cvt_pk_bf16_f32 v4, v15, v17
	v_cvt_pk_bf16_f32 v5, v19, v21
	ds_read2_b32 v[8:9], v185 offset0:81 offset1:89
	ds_read2_b32 v[10:11], v185 offset0:16 offset1:24
	ds_read2_b32 v[12:13], v185 offset0:146 offset1:154
	ds_read2_b32 v[14:15], v185 offset0:211 offset1:219
	ds_read2_b32 v[16:17], v26 offset0:20 offset1:28
	ds_read2_b32 v[18:19], v26 offset0:85 offset1:93
	ds_read2_b32 v[20:21], v26 offset0:150 offset1:158
	ds_read2_b32 v[24:25], v26 offset0:215 offset1:223
	v_lshl_add_u64 v[6:7], v[22:23], 0, v[74:75]
	global_store_dwordx4 v[6:7], v[2:5], off nt
	v_lshl_add_u64 v[6:7], v[22:23], 0, v[80:81]
	s_waitcnt lgkmcnt(6)
	v_cvt_pk_bf16_f32 v2, v10, v8
	s_waitcnt lgkmcnt(4)
	v_cvt_pk_bf16_f32 v3, v12, v14
	s_waitcnt lgkmcnt(2)
	v_cvt_pk_bf16_f32 v4, v16, v18
	s_waitcnt lgkmcnt(0)
	v_cvt_pk_bf16_f32 v5, v20, v24
	global_store_dwordx4 v[6:7], v[2:5], off nt
	v_lshl_add_u64 v[6:7], v[22:23], 0, v[86:87]
	s_nop 0
	v_cvt_pk_bf16_f32 v2, v11, v9
	v_cvt_pk_bf16_f32 v3, v13, v15
	v_cvt_pk_bf16_f32 v4, v17, v19
	v_cvt_pk_bf16_f32 v5, v21, v25
	ds_read2_b32 v[8:9], v185 offset0:32 offset1:40
	ds_read2_b32 v[10:11], v185 offset0:97 offset1:105
	ds_read2_b32 v[12:13], v185 offset0:162 offset1:170
	ds_read2_b32 v[14:15], v185 offset0:227 offset1:235
	ds_read2_b32 v[16:17], v26 offset0:36 offset1:44
	ds_read2_b32 v[18:19], v26 offset0:101 offset1:109
	ds_read2_b32 v[20:21], v26 offset0:166 offset1:174
	ds_read2_b32 v[24:25], v26 offset0:231 offset1:239
	global_store_dwordx4 v[6:7], v[2:5], off nt
	v_lshl_add_u64 v[6:7], v[22:23], 0, v[90:91]
	s_waitcnt lgkmcnt(6)
	v_cvt_pk_bf16_f32 v2, v8, v10
	s_waitcnt lgkmcnt(4)
	v_cvt_pk_bf16_f32 v3, v12, v14
	s_waitcnt lgkmcnt(2)
	v_cvt_pk_bf16_f32 v4, v16, v18
	s_waitcnt lgkmcnt(0)
	v_cvt_pk_bf16_f32 v5, v20, v24
	global_store_dwordx4 v[6:7], v[2:5], off nt
	v_lshl_add_u64 v[6:7], v[22:23], 0, v[94:95]
	s_nop 0
	v_cvt_pk_bf16_f32 v2, v9, v11
	v_cvt_pk_bf16_f32 v3, v13, v15
	v_cvt_pk_bf16_f32 v4, v17, v19
	v_cvt_pk_bf16_f32 v5, v21, v25
	ds_read2_b32 v[8:9], v185 offset0:48 offset1:56
	ds_read2_b32 v[10:11], v185 offset0:113 offset1:121
	ds_read2_b32 v[12:13], v185 offset0:178 offset1:186
	ds_read2_b32 v[14:15], v185 offset0:243 offset1:251
	ds_read2_b32 v[16:17], v26 offset0:52 offset1:60
	ds_read2_b32 v[18:19], v26 offset0:117 offset1:125
	ds_read2_b32 v[20:21], v26 offset0:182 offset1:190
	ds_read2_b32 v[24:25], v26 offset0:247 offset1:255
	global_store_dwordx4 v[6:7], v[2:5], off nt
	v_lshl_add_u64 v[6:7], v[22:23], 0, v[98:99]
	s_waitcnt lgkmcnt(6)
	v_cvt_pk_bf16_f32 v2, v8, v10
	s_waitcnt lgkmcnt(4)
	v_cvt_pk_bf16_f32 v3, v12, v14
	s_waitcnt lgkmcnt(2)
	v_cvt_pk_bf16_f32 v4, v16, v18
	s_waitcnt lgkmcnt(0)
	v_cvt_pk_bf16_f32 v5, v20, v24
	global_store_dwordx4 v[6:7], v[2:5], off nt
	v_lshl_add_u64 v[6:7], v[22:23], 0, v[102:103]
	s_nop 0
	v_cvt_pk_bf16_f32 v2, v9, v11
	v_cvt_pk_bf16_f32 v3, v13, v15
	v_cvt_pk_bf16_f32 v4, v17, v19
	v_cvt_pk_bf16_f32 v5, v21, v25
	global_store_dwordx4 v[6:7], v[2:5], off nt
	s_waitcnt lgkmcnt(0)

.LBB0_25:
	s_andn2_b64 vcc, exec, s[18:19]
	s_cbranch_vccnz .LBB0_27
	s_add_i32 s2, s20, 0xfffff900
	s_lshr_b32 s2, s2, 6
	s_lshl_b32 s17, s16, 2
	s_add_i32 s18, s2, s17
	s_ashr_i32 s19, s18, 31
	s_and_b32 s2, s46, 0xc0
	s_lshl_b64 s[22:23], s[18:19], 20
	s_waitcnt lgkmcnt(0)
	s_add_u32 s17, s8, s22
	s_addc_u32 s21, s9, s23
	s_lshl_b32 s22, s2, 12
	s_add_u32 s17, s17, s22
	s_addc_u32 s21, s21, 0
	s_and_b32 s24, s45, 0x3c0
	s_lshl_b32 s22, s24, 2
	s_add_u32 s22, s17, s22
	s_addc_u32 s23, s21, 0
	v_lshlrev_b32_e32 v66, 2, v118
	v_lshl_add_u64 v[62:63], s[22:23], 0, v[66:67]
	v_lshl_add_u64 v[2:3], v[62:63], 0, v[120:121]
	global_load_dwordx4 v[2:5], v[2:3], off nt
	v_lshl_add_u64 v[34:35], v[62:63], 0, v[152:153]
	v_lshl_add_u64 v[38:39], v[62:63], 0, v[156:157]
	v_lshl_add_u64 v[6:7], v[62:63], 0, v[124:125]
	global_load_dwordx4 v[34:37], v[34:35], off nt
	v_lshl_add_u64 v[42:43], v[62:63], 0, v[160:161]
	global_load_dwordx4 v[38:41], v[38:39], off nt
	v_lshl_add_u64 v[10:11], v[62:63], 0, v[128:129]
	global_load_dwordx4 v[6:9], v[6:7], off nt
	v_lshl_add_u64 v[46:47], v[62:63], 0, v[164:165]
	global_load_dwordx4 v[42:45], v[42:43], off nt
	v_lshl_add_u64 v[14:15], v[62:63], 0, v[132:133]
	global_load_dwordx4 v[10:13], v[10:11], off nt
	v_lshl_add_u64 v[50:51], v[62:63], 0, v[168:169]
	global_load_dwordx4 v[46:49], v[46:47], off nt
	v_lshl_add_u64 v[18:19], v[62:63], 0, v[136:137]
	global_load_dwordx4 v[14:17], v[14:15], off nt
	v_lshl_add_u64 v[54:55], v[62:63], 0, v[172:173]
	global_load_dwordx4 v[50:53], v[50:51], off nt
	v_lshl_add_u64 v[22:23], v[62:63], 0, v[140:141]
	global_load_dwordx4 v[18:21], v[18:19], off nt
	v_lshl_add_u64 v[58:59], v[62:63], 0, v[176:177]
	global_load_dwordx4 v[54:57], v[54:55], off nt
	v_lshl_add_u64 v[26:27], v[62:63], 0, v[144:145]
	global_load_dwordx4 v[22:25], v[22:23], off nt
	v_lshl_add_u64 v[30:31], v[62:63], 0, v[148:149]
	global_load_dwordx4 v[58:61], v[58:59], off nt
	v_lshl_add_u64 v[62:63], v[62:63], 0, v[180:181]
	global_load_dwordx4 v[26:29], v[26:27], off nt
	v_add_u32_e32 v66, v189, v188
	global_load_dwordx4 v[62:65], v[62:63], off nt
	v_add_u32_e32 v186, 0x410, v66
	global_load_dwordx4 v[30:33], v[30:31], off nt
	v_add_u32_e32 v187, 0x418, v66
	v_add_u32_e32 v190, 0x820, v66
	v_add_u32_e32 v191, 0x828, v66
	v_add_u32_e32 v192, 0xc30, v66
	v_add_u32_e32 v193, 0xc38, v66
	v_add_u32_e32 v194, 0x1040, v66
	v_add_u32_e32 v195, 0x1048, v66
	v_add_u32_e32 v196, 0x1450, v66
	v_add_u32_e32 v197, 0x1458, v66
	v_add_u32_e32 v198, 0x1860, v66
	v_add_u32_e32 v199, 0x1868, v66
	v_add_u32_e32 v200, 0x1c70, v66
	v_add_u32_e32 v201, 0x1c78, v66
	v_add_u32_e32 v202, 0x2080, v66
	v_add_u32_e32 v203, 0x2088, v66
	v_add_u32_e32 v204, 0x2490, v66
	s_lshl_b64 s[18:19], s[18:19], 19
	s_add_u32 s17, s38, s18
	s_addc_u32 s18, s39, s19
	s_lshl_b32 s19, s24, 9
	s_add_u32 s17, s17, s19
	s_addc_u32 s19, s18, 0
	s_lshl_b32 s2, s2, 1
	s_add_u32 s18, s17, s2
	s_addc_u32 s19, s19, 0
	s_waitcnt vmcnt(15)
	ds_write2_b32 v66, v2, v3 offset1:1
	ds_write2_b32 v66, v4, v5 offset0:2 offset1:3
	s_waitcnt vmcnt(12)
	ds_write2_b32 v186, v6, v7 offset1:1
	ds_write2_b32 v187, v8, v9 offset1:1
	s_waitcnt vmcnt(10)
	ds_write2_b32 v190, v10, v11 offset1:1
	ds_write2_b32 v191, v12, v13 offset1:1
	s_waitcnt vmcnt(8)
	ds_write2_b32 v192, v14, v15 offset1:1
	ds_write2_b32 v193, v16, v17 offset1:1
	s_waitcnt vmcnt(6)
	ds_write2_b32 v194, v18, v19 offset1:1
	ds_write2_b32 v195, v20, v21 offset1:1
	s_waitcnt vmcnt(4)
	ds_write2_b32 v196, v22, v23 offset1:1
	ds_write2_b32 v197, v24, v25 offset1:1
	s_waitcnt vmcnt(2)
	ds_write2_b32 v198, v26, v27 offset1:1
	ds_write2_b32 v199, v28, v29 offset1:1
	s_waitcnt vmcnt(0)
	ds_write2_b32 v200, v30, v31 offset1:1
	ds_write2_b32 v201, v32, v33 offset1:1
	ds_write2_b32 v202, v34, v35 offset1:1
	ds_write2_b32 v203, v36, v37 offset1:1
	ds_write2_b32 v204, v38, v39 offset1:1
	v_add_u32_e32 v2, 0x2498, v66
	ds_write2_b32 v2, v40, v41 offset1:1
	v_add_u32_e32 v2, 0x28a0, v66
	ds_write2_b32 v2, v42, v43 offset1:1
	v_add_u32_e32 v2, 0x28a8, v66
	ds_write2_b32 v2, v44, v45 offset1:1
	v_add_u32_e32 v2, 0x2cb0, v66
	ds_write2_b32 v2, v46, v47 offset1:1
	v_add_u32_e32 v2, 0x2cb8, v66
	ds_write2_b32 v2, v48, v49 offset1:1
	v_add_u32_e32 v2, 0x30c0, v66
	ds_write2_b32 v2, v50, v51 offset1:1
	v_add_u32_e32 v2, 0x30c8, v66
	ds_write2_b32 v2, v52, v53 offset1:1
	v_add_u32_e32 v2, 0x34d0, v66
	ds_write2_b32 v2, v54, v55 offset1:1
	v_add_u32_e32 v2, 0x34d8, v66
	ds_write2_b32 v2, v56, v57 offset1:1
	v_add_u32_e32 v2, 0x38e0, v66
	ds_write2_b32 v2, v58, v59 offset1:1
	v_add_u32_e32 v2, 0x38e8, v66
	ds_write2_b32 v2, v60, v61 offset1:1
	v_add_u32_e32 v2, 0x3cf0, v66
	ds_write2_b32 v2, v62, v63 offset1:1
	v_add_u32_e32 v2, 0x3cf8, v66
	ds_write2_b32 v2, v64, v65 offset1:1
	s_waitcnt lgkmcnt(0)
	v_add_u32_e32 v26, 0x400, v185
	ds_read2_b32 v[6:7], v185 offset0:65 offset1:73
	ds_read2_b32 v[8:9], v185 offset1:8
	ds_read2_b32 v[10:11], v185 offset0:130 offset1:138
	ds_read2_b32 v[12:13], v185 offset0:195 offset1:203
	ds_read2_b32 v[14:15], v26 offset0:4 offset1:12
	ds_read2_b32 v[16:17], v26 offset0:69 offset1:77
	ds_read2_b32 v[18:19], v26 offset0:134 offset1:142
	ds_read2_b32 v[20:21], v26 offset0:199 offset1:207
	v_lshlrev_b32_e32 v66, 1, v70
	v_lshl_add_u64 v[22:23], s[18:19], 0, v[66:67]
	s_waitcnt lgkmcnt(6)
	v_cvt_pk_bf16_f32 v2, v8, v6
	s_waitcnt lgkmcnt(4)
	v_cvt_pk_bf16_f32 v3, v10, v12
	s_waitcnt lgkmcnt(2)
	v_cvt_pk_bf16_f32 v4, v14, v16
	s_waitcnt lgkmcnt(0)
	v_cvt_pk_bf16_f32 v5, v18, v20
	v_lshl_add_u64 v[24:25], v[22:23], 0, v[114:115]
	global_store_dwordx4 v[24:25], v[2:5], off nt
	s_nop 1
	v_cvt_pk_bf16_f32 v2, v9, v7
	v_cvt_pk_bf16_f32 v3, v11, v13
	v_cvt_pk_bf16_f32 v4, v15, v17
	v_cvt_pk_bf16_f32 v5, v19, v21
	ds_read2_b32 v[8:9], v185 offset0:81 offset1:89
	ds_read2_b32 v[10:11], v185 offset0:16 offset1:24
	ds_read2_b32 v[12:13], v185 offset0:146 offset1:154
	ds_read2_b32 v[14:15], v185 offset0:211 offset1:219
	ds_read2_b32 v[16:17], v26 offset0:20 offset1:28
	ds_read2_b32 v[18:19], v26 offset0:85 offset1:93
	ds_read2_b32 v[20:21], v26 offset0:150 offset1:158
	ds_read2_b32 v[24:25], v26 offset0:215 offset1:223
	v_lshl_add_u64 v[6:7], v[22:23], 0, v[76:77]
	global_store_dwordx4 v[6:7], v[2:5], off nt
	v_lshl_add_u64 v[6:7], v[22:23], 0, v[82:83]
	s_waitcnt lgkmcnt(6)
	v_cvt_pk_bf16_f32 v2, v10, v8
	s_waitcnt lgkmcnt(4)
	v_cvt_pk_bf16_f32 v3, v12, v14
	s_waitcnt lgkmcnt(2)
	v_cvt_pk_bf16_f32 v4, v16, v18
	s_waitcnt lgkmcnt(0)
	v_cvt_pk_bf16_f32 v5, v20, v24
	global_store_dwordx4 v[6:7], v[2:5], off nt
	v_lshl_add_u64 v[6:7], v[22:23], 0, v[88:89]
	s_nop 0
	v_cvt_pk_bf16_f32 v2, v11, v9
	v_cvt_pk_bf16_f32 v3, v13, v15
	v_cvt_pk_bf16_f32 v4, v17, v19
	v_cvt_pk_bf16_f32 v5, v21, v25
	ds_read2_b32 v[8:9], v185 offset0:32 offset1:40
	ds_read2_b32 v[10:11], v185 offset0:97 offset1:105
	ds_read2_b32 v[12:13], v185 offset0:162 offset1:170
	ds_read2_b32 v[14:15], v185 offset0:227 offset1:235
	ds_read2_b32 v[16:17], v26 offset0:36 offset1:44
	ds_read2_b32 v[18:19], v26 offset0:101 offset1:109
	ds_read2_b32 v[20:21], v26 offset0:166 offset1:174
	ds_read2_b32 v[24:25], v26 offset0:231 offset1:239
	global_store_dwordx4 v[6:7], v[2:5], off nt
	v_lshl_add_u64 v[6:7], v[22:23], 0, v[92:93]
	s_waitcnt lgkmcnt(6)
	v_cvt_pk_bf16_f32 v2, v8, v10
	s_waitcnt lgkmcnt(4)
	v_cvt_pk_bf16_f32 v3, v12, v14
	s_waitcnt lgkmcnt(2)
	v_cvt_pk_bf16_f32 v4, v16, v18
	s_waitcnt lgkmcnt(0)
	v_cvt_pk_bf16_f32 v5, v20, v24
	global_store_dwordx4 v[6:7], v[2:5], off nt
	v_lshl_add_u64 v[6:7], v[22:23], 0, v[96:97]
	s_nop 0
	v_cvt_pk_bf16_f32 v2, v9, v11
	v_cvt_pk_bf16_f32 v3, v13, v15
	v_cvt_pk_bf16_f32 v4, v17, v19
	v_cvt_pk_bf16_f32 v5, v21, v25
	ds_read2_b32 v[8:9], v185 offset0:48 offset1:56
	ds_read2_b32 v[10:11], v185 offset0:113 offset1:121
	ds_read2_b32 v[12:13], v185 offset0:178 offset1:186
	ds_read2_b32 v[14:15], v185 offset0:243 offset1:251
	ds_read2_b32 v[16:17], v26 offset0:52 offset1:60
	ds_read2_b32 v[18:19], v26 offset0:117 offset1:125
	ds_read2_b32 v[20:21], v26 offset0:182 offset1:190
	ds_read2_b32 v[24:25], v26 offset0:247 offset1:255
	global_store_dwordx4 v[6:7], v[2:5], off nt
	v_lshl_add_u64 v[6:7], v[22:23], 0, v[100:101]
	s_waitcnt lgkmcnt(6)
	v_cvt_pk_bf16_f32 v2, v8, v10
	s_waitcnt lgkmcnt(4)
	v_cvt_pk_bf16_f32 v3, v12, v14
	s_waitcnt lgkmcnt(2)
	v_cvt_pk_bf16_f32 v4, v16, v18
	s_waitcnt lgkmcnt(0)
	v_cvt_pk_bf16_f32 v5, v20, v24
	global_store_dwordx4 v[6:7], v[2:5], off nt
	v_lshl_add_u64 v[6:7], v[22:23], 0, v[104:105]
	s_nop 0
	v_cvt_pk_bf16_f32 v2, v9, v11
	v_cvt_pk_bf16_f32 v3, v13, v15
	v_cvt_pk_bf16_f32 v4, v17, v19
	v_cvt_pk_bf16_f32 v5, v21, v25
	global_store_dwordx4 v[6:7], v[2:5], off nt
	s_waitcnt lgkmcnt(0)

.LBB0_28:
	s_andn2_b64 vcc, exec, s[18:19]
	s_cbranch_vccnz .LBB0_13
	s_mul_hi_i32 s2, s20, 0x92492493
	s_add_i32 s2, s2, s20
	s_lshr_b32 s17, s2, 31
	s_ashr_i32 s19, s2, 6
	s_add_i32 s19, s19, s17
	s_mul_i32 s2, s19, 0xffffff90
	s_mul_i32 s17, s16, 0x6900
	s_sub_i32 s2, s2, s17
	s_add_i32 s86, s30, s2
	s_lshl_b32 s18, s86, 6
	s_add_i32 s2, s18, 0xffffff10
	s_cmp_gt_u32 s86, 47
	s_cselect_b32 s2, s2, 0
	s_cmp_eq_u32 s86, 44
	s_cselect_b64 s[20:21], -1, 0
	s_and_b64 s[22:23], s[20:21], exec
	s_cselect_b32 s22, 0xb00, s2
	s_mov_b64 s[24:25], -1
	s_cmp_gt_i32 s86, 47
	s_mul_hi_i32 s87, s16, 0x1b10000
	s_mul_i32 s88, s16, 0x1b10000
	s_cbranch_scc0 .LBB0_31
	s_lshl_b32 s2, s19, 6
	s_and_b32 s25, s2, 0xffffff80
	s_lshl_b32 s2, s19, 5
	s_and_b32 s2, s2, 32
	s_ashr_i32 s17, s16, 31
	s_waitcnt lgkmcnt(0)
	s_add_u32 s23, s14, s88
	s_addc_u32 s89, s15, s87
	s_ashr_i32 s24, s25, 31
	s_mul_i32 s91, s25, 0x6c40
	s_mul_hi_i32 s90, s25, 0x6c40
	s_add_u32 s96, s23, s91
	s_addc_u32 s89, s89, s90
	s_ashr_i32 s23, s22, 31
	s_lshl_b64 s[90:91], s[22:23], 2
	s_add_u32 s23, s96, s90
	s_addc_u32 s89, s89, s91
	s_lshl_b32 s90, s2, 2
	s_add_u32 s90, s23, s90
	s_addc_u32 s91, s89, 0
	v_lshl_add_u64 v[2:3], s[90:91], 0, v[116:117]
	v_lshlrev_b32_e32 v66, 2, v184
	v_lshl_add_u64 v[62:63], v[2:3], 0, v[66:67]
	v_add_co_u32_e32 v6, vcc, s71, v62
	s_lshl_b64 s[90:91], s[16:17], 22
	s_nop 0
	v_addc_co_u32_e32 v7, vcc, 0, v63, vcc
	v_add_co_u32_e32 v10, vcc, s72, v62
	global_load_dwordx4 v[2:5], v[62:63], off nt
	s_nop 0
	global_load_dwordx4 v[6:9], v[6:7], off offset:512 nt
	v_addc_co_u32_e32 v11, vcc, 0, v63, vcc
	v_add_co_u32_e32 v14, vcc, s73, v62
	s_add_u32 s17, s40, s90
	s_nop 0
	v_addc_co_u32_e32 v15, vcc, 0, v63, vcc
	global_load_dwordx4 v[10:13], v[10:11], off offset:1024 nt
	s_nop 0
	global_load_dwordx4 v[14:17], v[14:15], off offset:1536 nt
	v_add_co_u32_e32 v18, vcc, s74, v62
	s_addc_u32 s23, s41, s91
	s_nop 0
	v_addc_co_u32_e32 v19, vcc, 0, v63, vcc
	v_add_co_u32_e32 v22, vcc, s75, v62
	s_add_i32 s2, s18, s2
	s_nop 0
	v_addc_co_u32_e32 v23, vcc, 0, v63, vcc
	global_load_dwordx4 v[18:21], v[18:19], off offset:2048 nt
	s_nop 0
	global_load_dwordx4 v[22:25], v[22:23], off offset:2560 nt
	v_add_co_u32_e32 v26, vcc, s76, v62
	s_addk_i32 s2, 0xf400
	s_nop 0
	v_addc_co_u32_e32 v27, vcc, 0, v63, vcc
	v_add_co_u32_e32 v30, vcc, s77, v62
	s_lshl_b64 s[90:91], s[2:3], 10
	s_nop 0
	v_addc_co_u32_e32 v31, vcc, 0, v63, vcc
	global_load_dwordx4 v[26:29], v[26:27], off offset:3072 nt
	s_nop 0
	global_load_dwordx4 v[30:33], v[30:31], off offset:3584 nt
	v_add_co_u32_e32 v34, vcc, s78, v62
	s_add_u32 s2, s17, s90
	s_nop 0
	v_addc_co_u32_e32 v35, vcc, 0, v63, vcc
	v_add_co_u32_e32 v38, vcc, s79, v62
	s_addc_u32 s17, s23, s91
	s_nop 0
	v_addc_co_u32_e32 v39, vcc, 0, v63, vcc
	global_load_dwordx4 v[34:37], v[34:35], off nt
	s_nop 0
	global_load_dwordx4 v[38:41], v[38:39], off offset:512 nt
	v_add_co_u32_e32 v42, vcc, s80, v62
	s_add_u32 s90, s2, s25
	s_nop 0
	v_addc_co_u32_e32 v43, vcc, 0, v63, vcc
	v_add_co_u32_e32 v46, vcc, s81, v62
	s_addc_u32 s91, s17, s24
	s_nop 0
	v_addc_co_u32_e32 v47, vcc, 0, v63, vcc
	global_load_dwordx4 v[42:45], v[42:43], off offset:1024 nt
	s_nop 0
	global_load_dwordx4 v[46:49], v[46:47], off offset:1536 nt
	v_add_co_u32_e32 v50, vcc, s82, v62
	s_mov_b64 s[24:25], 0
	s_nop 0
	v_addc_co_u32_e32 v51, vcc, 0, v63, vcc
	global_load_dwordx4 v[50:53], v[50:51], off offset:2048 nt
	v_add_co_u32_e32 v54, vcc, s83, v62
	s_nop 1
	v_addc_co_u32_e32 v55, vcc, 0, v63, vcc
	global_load_dwordx4 v[54:57], v[54:55], off offset:2560 nt
	v_add_co_u32_e32 v58, vcc, s84, v62
	s_nop 1
	v_addc_co_u32_e32 v59, vcc, 0, v63, vcc
	global_load_dwordx4 v[58:61], v[58:59], off offset:3072 nt
	v_add_co_u32_e32 v62, vcc, s85, v62
	s_nop 1
	v_addc_co_u32_e32 v63, vcc, 0, v63, vcc
	global_load_dwordx4 v[62:65], v[62:63], off offset:3584 nt
	s_waitcnt vmcnt(15)
	ds_write2_b32 v71, v2, v3 offset1:1
	ds_write2_b32 v71, v4, v5 offset0:2 offset1:3
	v_add_u32_e32 v2, 0x420, v71
	s_waitcnt vmcnt(14)
	ds_write2_b32 v2, v6, v7 offset1:1
	v_add_u32_e32 v2, 0x428, v71
	ds_write2_b32 v2, v8, v9 offset1:1
	v_add_u32_e32 v2, 0x840, v71
	s_waitcnt vmcnt(13)
	ds_write2_b32 v2, v10, v11 offset1:1
	v_add_u32_e32 v2, 0x848, v71
	ds_write2_b32 v2, v12, v13 offset1:1
	v_add_u32_e32 v2, 0xc60, v71
	s_waitcnt vmcnt(12)
	ds_write2_b32 v2, v14, v15 offset1:1
	v_add_u32_e32 v2, 0xc68, v71
	ds_write2_b32 v2, v16, v17 offset1:1
	v_add_u32_e32 v2, 0x1080, v71
	s_waitcnt vmcnt(11)
	ds_write2_b32 v2, v18, v19 offset1:1
	v_add_u32_e32 v2, 0x1088, v71
	ds_write2_b32 v2, v20, v21 offset1:1
	v_add_u32_e32 v2, 0x14a0, v71
	s_waitcnt vmcnt(10)
	ds_write2_b32 v2, v22, v23 offset1:1
	v_add_u32_e32 v2, 0x14a8, v71
	ds_write2_b32 v2, v24, v25 offset1:1
	v_add_u32_e32 v2, 0x18c0, v71
	s_waitcnt vmcnt(9)
	ds_write2_b32 v2, v26, v27 offset1:1
	v_add_u32_e32 v2, 0x18c8, v71
	ds_write2_b32 v2, v28, v29 offset1:1
	v_add_u32_e32 v2, 0x1ce0, v71
	s_waitcnt vmcnt(8)
	ds_write2_b32 v2, v30, v31 offset1:1
	v_add_u32_e32 v2, 0x1ce8, v71
	ds_write2_b32 v2, v32, v33 offset1:1
	v_add_u32_e32 v2, 0x2100, v71
	s_waitcnt vmcnt(7)
	ds_write2_b32 v2, v34, v35 offset1:1
	v_add_u32_e32 v2, 0x2108, v71
	ds_write2_b32 v2, v36, v37 offset1:1
	v_add_u32_e32 v2, 0x2520, v71
	s_waitcnt vmcnt(6)
	ds_write2_b32 v2, v38, v39 offset1:1
	v_add_u32_e32 v2, 0x2528, v71
	ds_write2_b32 v2, v40, v41 offset1:1
	v_add_u32_e32 v2, 0x2940, v71
	v_lshl_add_u64 v[38:39], s[90:91], 0, v[68:69]
	v_lshl_add_u64 v[40:41], v[38:39], 0, v[108:109]
	s_waitcnt vmcnt(5)
	ds_write2_b32 v2, v42, v43 offset1:1
	v_add_u32_e32 v2, 0x2948, v71
	ds_write2_b32 v2, v44, v45 offset1:1
	v_add_u32_e32 v2, 0x2d60, v71
	s_waitcnt vmcnt(4)
	ds_write2_b32 v2, v46, v47 offset1:1
	v_add_u32_e32 v2, 0x2d68, v71
	ds_write2_b32 v2, v48, v49 offset1:1
	v_add_u32_e32 v2, 0x3180, v71
	s_waitcnt vmcnt(3)
	ds_write2_b32 v2, v50, v51 offset1:1
	v_add_u32_e32 v2, 0x3188, v71
	ds_write2_b32 v2, v52, v53 offset1:1
	v_add_u32_e32 v2, 0x35a0, v71
	v_add_u32_e32 v42, 0x400, v119
	s_waitcnt vmcnt(2)
	ds_write2_b32 v2, v54, v55 offset1:1
	v_add_u32_e32 v2, 0x35a8, v71
	ds_write2_b32 v2, v56, v57 offset1:1
	v_add_u32_e32 v2, 0x39c0, v71
	s_waitcnt vmcnt(1)
	ds_write2_b32 v2, v58, v59 offset1:1
	v_add_u32_e32 v2, 0x39c8, v71
	ds_write2_b32 v2, v60, v61 offset1:1
	v_add_u32_e32 v2, 0x3de0, v71
	s_waitcnt vmcnt(0)
	ds_write2_b32 v2, v62, v63 offset1:1
	v_add_u32_e32 v2, 0x3de8, v71
	ds_write2_b32 v2, v64, v65 offset1:1
	s_waitcnt lgkmcnt(0)
	ds_read2_b32 v[6:7], v119 offset0:66 offset1:74
	ds_read2_b32 v[8:9], v119 offset0:99 offset1:107
	ds_read2_b32 v[10:11], v119 offset1:8
	ds_read2_b32 v[12:13], v119 offset0:33 offset1:41
	v_mov_b32_e32 v2, v67
	s_waitcnt lgkmcnt(3)
	v_mul_f32_e32 v3, 0x42000000, v6
	ds_read2_b32 v[14:15], v119 offset0:198 offset1:206
	ds_read2_b32 v[16:17], v119 offset0:231 offset1:239
	ds_read2_b32 v[18:19], v119 offset0:132 offset1:140
	ds_read2_b32 v[20:21], v119 offset0:165 offset1:173
	s_waitcnt lgkmcnt(5)
	v_mul_f32_e32 v5, 0x42000000, v10
	s_waitcnt lgkmcnt(4)
	v_mul_f32_e32 v6, 0x42000000, v12
	v_cvt_pk_fp8_f32 v2, v5, v6
	v_mul_f32_e32 v4, 0x42000000, v8
	s_waitcnt lgkmcnt(1)
	v_mul_f32_e32 v6, 0x42000000, v18
	s_waitcnt lgkmcnt(0)
	v_mul_f32_e32 v8, 0x42000000, v20
	v_cvt_pk_fp8_f32 v2, v3, v4 op_sel:[0,0,1]
	v_mov_b32_e32 v3, v67
	ds_read2_b32 v[22:23], v42 offset0:74 offset1:82
	ds_read2_b32 v[24:25], v42 offset0:107 offset1:115
	ds_read2_b32 v[26:27], v42 offset0:8 offset1:16
	ds_read2_b32 v[28:29], v42 offset0:41 offset1:49
	v_cvt_pk_fp8_f32 v3, v6, v8
	ds_read2_b32 v[30:31], v42 offset0:140 offset1:148
	ds_read2_b32 v[32:33], v42 offset0:173 offset1:181
	v_mul_f32_e32 v4, 0x42000000, v14
	v_mul_f32_e32 v5, 0x42000000, v16
	v_cvt_pk_fp8_f32 v3, v4, v5 op_sel:[0,0,1]
	s_waitcnt lgkmcnt(3)
	v_mul_f32_e32 v5, 0x42000000, v26
	s_waitcnt lgkmcnt(2)
	v_mul_f32_e32 v10, 0x42000000, v28
	v_mov_b32_e32 v4, v67
	ds_read2_b32 v[34:35], v42 offset0:206 offset1:214
	ds_read2_b32 v[36:37], v42 offset0:239 offset1:247
	v_cvt_pk_fp8_f32 v4, v5, v10
	s_waitcnt lgkmcnt(3)
	v_mul_f32_e32 v10, 0x42000000, v30
	s_waitcnt lgkmcnt(2)
	v_mul_f32_e32 v12, 0x42000000, v32
	v_mov_b32_e32 v5, v67
	v_cvt_pk_fp8_f32 v5, v10, v12
	v_mul_f32_e32 v6, 0x42000000, v22
	v_mul_f32_e32 v8, 0x42000000, v24
	v_cvt_pk_fp8_f32 v4, v6, v8 op_sel:[0,0,1]
	s_waitcnt lgkmcnt(1)
	v_mul_f32_e32 v6, 0x42000000, v34
	s_waitcnt lgkmcnt(0)
	v_mul_f32_e32 v8, 0x42000000, v36
	v_cvt_pk_fp8_f32 v5, v6, v8 op_sel:[0,0,1]
	v_mul_f32_e32 v6, 0x42000000, v13
	v_mul_f32_e32 v8, 0x42000000, v29
	global_store_dwordx4 v[40:41], v[2:5], off nt
	s_nop 1
	v_mul_f32_e32 v3, 0x42000000, v11
	v_mov_b32_e32 v2, v67
	v_mul_f32_e32 v4, 0x42000000, v7
	v_cvt_pk_fp8_f32 v2, v3, v6
	v_mul_f32_e32 v6, 0x42000000, v19
	v_mul_f32_e32 v7, 0x42000000, v21
	v_mov_b32_e32 v3, v67
	v_cvt_pk_fp8_f32 v3, v6, v7
	v_mul_f32_e32 v5, 0x42000000, v9
	v_cvt_pk_fp8_f32 v2, v4, v5 op_sel:[0,0,1]
	v_mul_f32_e32 v4, 0x42000000, v15
	v_mul_f32_e32 v5, 0x42000000, v17
	v_cvt_pk_fp8_f32 v3, v4, v5 op_sel:[0,0,1]
	v_mul_f32_e32 v5, 0x42000000, v27
	v_mov_b32_e32 v4, v67
	v_cvt_pk_fp8_f32 v4, v5, v8
	v_mul_f32_e32 v8, 0x42000000, v31
	v_mul_f32_e32 v9, 0x42000000, v33
	v_mov_b32_e32 v5, v67
	v_cvt_pk_fp8_f32 v5, v8, v9
	v_mul_f32_e32 v6, 0x42000000, v23
	v_mul_f32_e32 v7, 0x42000000, v25
	v_cvt_pk_fp8_f32 v4, v6, v7 op_sel:[0,0,1]
	v_mul_f32_e32 v6, 0x42000000, v35
	v_mul_f32_e32 v7, 0x42000000, v37
	ds_read2_b32 v[8:9], v119 offset0:82 offset1:90
	ds_read2_b32 v[10:11], v119 offset0:115 offset1:123
	ds_read2_b32 v[12:13], v119 offset0:16 offset1:24
	ds_read2_b32 v[14:15], v119 offset0:49 offset1:57
	v_cvt_pk_fp8_f32 v5, v6, v7 op_sel:[0,0,1]
	v_lshl_add_u64 v[6:7], v[38:39], 0, v[72:73]
	global_store_dwordx4 v[6:7], v[2:5], off nt
	s_waitcnt lgkmcnt(1)
	s_nop 0
	v_mul_f32_e32 v5, 0x42000000, v12
	s_waitcnt lgkmcnt(0)
	v_mul_f32_e32 v6, 0x42000000, v14
	v_mov_b32_e32 v2, v67
	v_cvt_pk_fp8_f32 v2, v5, v6
	ds_read2_b32 v[16:17], v119 offset0:214 offset1:222
	ds_read2_b32 v[18:19], v119 offset0:247 offset1:255
	ds_read2_b32 v[6:7], v119 offset0:148 offset1:156
	ds_read2_b32 v[20:21], v119 offset0:181 offset1:189
	v_mul_f32_e32 v3, 0x42000000, v8
	v_mul_f32_e32 v4, 0x42000000, v10
	v_cvt_pk_fp8_f32 v2, v3, v4 op_sel:[0,0,1]
	s_waitcnt lgkmcnt(1)
	v_mul_f32_e32 v6, 0x42000000, v6
	s_waitcnt lgkmcnt(0)
	v_mul_f32_e32 v8, 0x42000000, v20
	v_mov_b32_e32 v3, v67
	ds_read2_b32 v[22:23], v42 offset0:90 offset1:98
	ds_read2_b32 v[24:25], v42 offset0:123 offset1:131
	ds_read2_b32 v[26:27], v42 offset0:24 offset1:32
	ds_read2_b32 v[28:29], v42 offset0:57 offset1:65
	v_cvt_pk_fp8_f32 v3, v6, v8
	v_mul_f32_e32 v4, 0x42000000, v16
	v_mul_f32_e32 v5, 0x42000000, v18
	ds_read2_b32 v[30:31], v42 offset0:156 offset1:164
	ds_read2_b32 v[32:33], v42 offset0:189 offset1:197
	ds_read2_b32 v[34:35], v42 offset0:222 offset1:230
	v_cvt_pk_fp8_f32 v3, v4, v5 op_sel:[0,0,1]
	s_waitcnt lgkmcnt(4)
	v_mul_f32_e32 v5, 0x42000000, v26
	s_waitcnt lgkmcnt(3)
	v_mul_f32_e32 v10, 0x42000000, v28
	v_mov_b32_e32 v4, v67
	v_cvt_pk_fp8_f32 v4, v5, v10
	v_add_u32_e32 v5, 0x600, v119
	ds_read2_b32 v[36:37], v5 offset0:127 offset1:135
	s_waitcnt lgkmcnt(3)
	v_mul_f32_e32 v10, 0x42000000, v30
	s_waitcnt lgkmcnt(2)
	v_mul_f32_e32 v12, 0x42000000, v32
	v_mov_b32_e32 v5, v67
	v_cvt_pk_fp8_f32 v5, v10, v12
	v_mul_f32_e32 v6, 0x42000000, v22
	v_mul_f32_e32 v8, 0x42000000, v24
	v_cvt_pk_fp8_f32 v4, v6, v8 op_sel:[0,0,1]
	s_waitcnt lgkmcnt(1)
	v_mul_f32_e32 v6, 0x42000000, v34
	s_waitcnt lgkmcnt(0)
	v_mul_f32_e32 v8, 0x42000000, v36
	v_cvt_pk_fp8_f32 v5, v6, v8 op_sel:[0,0,1]
	v_mul_f32_e32 v8, 0x42000000, v9
	v_mul_f32_e32 v9, 0x42000000, v11
	v_mul_f32_e32 v10, 0x42000000, v13
	v_mul_f32_e32 v11, 0x42000000, v15
	v_mov_b32_e32 v6, v67
	v_cvt_pk_fp8_f32 v6, v10, v11
	v_mul_f32_e32 v10, 0x42000000, v7
	v_mul_f32_e32 v11, 0x42000000, v21
	v_mov_b32_e32 v7, v67
	v_cvt_pk_fp8_f32 v7, v10, v11
	v_cvt_pk_fp8_f32 v6, v8, v9 op_sel:[0,0,1]
	v_mul_f32_e32 v8, 0x42000000, v17
	v_mul_f32_e32 v9, 0x42000000, v19
	v_cvt_pk_fp8_f32 v7, v8, v9 op_sel:[0,0,1]
	v_mul_f32_e32 v9, 0x42000000, v27
	v_mul_f32_e32 v12, 0x42000000, v29
	v_mov_b32_e32 v8, v67
	v_cvt_pk_fp8_f32 v8, v9, v12
	v_mul_f32_e32 v12, 0x42000000, v31
	v_mul_f32_e32 v13, 0x42000000, v33
	v_mov_b32_e32 v9, v67
	v_cvt_pk_fp8_f32 v9, v12, v13
	v_mul_f32_e32 v10, 0x42000000, v23
	v_mul_f32_e32 v11, 0x42000000, v25
	v_cvt_pk_fp8_f32 v8, v10, v11 op_sel:[0,0,1]
	v_mul_f32_e32 v10, 0x42000000, v35
	v_mul_f32_e32 v11, 0x42000000, v37
	v_cvt_pk_fp8_f32 v9, v10, v11 op_sel:[0,0,1]
	v_lshl_add_u64 v[10:11], v[38:39], 0, v[78:79]
	global_store_dwordx4 v[10:11], v[2:5], off nt
	s_nop 1
	v_lshl_add_u64 v[2:3], v[38:39], 0, v[84:85]
	global_store_dwordx4 v[2:3], v[6:9], off nt
	s_waitcnt lgkmcnt(0)

.LBB0_1225:
	s_add_i32 s17, s16, 0x100
	s_add_i32 s2, s16, 0x102
	s_cmp_lt_i32 s17, s5
	s_cselect_b32 s10, s2, s17
	s_ashr_i32 s11, s10, 31
	s_lshl_b64 s[10:11], s[10:11], 4
	v_readlane_b32 s12, v252, 8
	v_readlane_b32 s13, v252, 9
	s_add_u32 s10, s12, s10
	s_addc_u32 s11, s13, s11
	global_load_dwordx4 v[16:19], v49, s[10:11] offset:16
	global_load_dwordx4 v[20:23], v49, s[10:11]
	s_mul_hi_i32 s2, s17, 0x78787879
	s_lshr_b32 s8, s2, 31
	s_ashr_i32 s2, s2, 11
	s_add_i32 s12, s2, s8
	s_mul_i32 s2, s12, 0xffffef00
	s_add_i32 s2, s16, s2
	s_add_i32 s8, s2, 0x100
	s_cmpk_gt_i32 s8, 0xff
	s_cselect_b64 s[14:15], -1, 0
	s_cmpk_lt_i32 s8, 0x100
	s_cbranch_scc1 .LBB0_1227
	s_waitcnt vmcnt(0)
	v_mov_b32_e32 v48, v44
	v_lshlrev_b64 v[72:73], 10, v[48:49]
	v_mov_b32_e32 v48, v45
	v_lshlrev_b64 v[44:45], 10, v[48:49]
	v_mov_b32_e32 v48, v46
	v_lshl_add_u64 v[88:89], v[52:53], 0, v[72:73]
	v_lshlrev_b64 v[72:73], 10, v[48:49]
	v_mov_b32_e32 v48, v47
	v_lshlrev_b64 v[46:47], 10, v[48:49]
	global_load_dwordx4 v[12:15], v[54:55], off nt
	global_load_dwordx4 v[8:11], v[54:55], off offset:1024 nt
	v_lshl_add_u64 v[44:45], v[52:53], 0, v[44:45]
	v_lshl_add_u64 v[90:91], v[52:53], 0, v[72:73]
	v_lshl_add_u64 v[46:47], v[52:53], 0, v[46:47]
	global_load_dwordx2 v[76:77], v[88:89], off nt
	global_load_dwordx2 v[74:75], v[44:45], off nt
	global_load_dwordx2 v[72:73], v[44:45], off offset:512 nt
	global_load_dwordx2 v[78:79], v[88:89], off offset:512 nt
	global_load_dwordx2 v[86:87], v[90:91], off nt
	global_load_dwordx2 v[84:85], v[46:47], off nt
	global_load_dwordx2 v[80:81], v[46:47], off offset:512 nt
	global_load_dwordx2 v[82:83], v[90:91], off offset:512 nt

.LBB0_1232:
	s_waitcnt vmcnt(0)
	v_mov_b32_e32 v48, v40
	v_lshlrev_b64 v[44:45], 10, v[48:49]
	v_mov_b32_e32 v48, v41
	v_lshlrev_b64 v[40:41], 10, v[48:49]
	v_mov_b32_e32 v48, v42
	v_lshlrev_b64 v[46:47], 10, v[48:49]
	v_mov_b32_e32 v48, v43
	v_lshl_add_u64 v[44:45], v[52:53], 0, v[44:45]
	v_lshlrev_b64 v[42:43], 10, v[48:49]
	global_load_dwordx4 v[4:7], v[54:55], off offset:2048 nt
	global_load_dwordx4 v[0:3], v[54:55], off offset:3072 nt
	v_lshl_add_u64 v[40:41], v[52:53], 0, v[40:41]
	v_lshl_add_u64 v[46:47], v[52:53], 0, v[46:47]
	v_lshl_add_u64 v[42:43], v[52:53], 0, v[42:43]
	global_load_dwordx2 v[60:61], v[44:45], off nt
	global_load_dwordx2 v[58:59], v[40:41], off nt
	global_load_dwordx2 v[56:57], v[40:41], off offset:512 nt
	global_load_dwordx2 v[62:63], v[44:45], off offset:512 nt
	global_load_dwordx2 v[70:71], v[46:47], off nt
	global_load_dwordx2 v[68:69], v[42:43], off nt
	global_load_dwordx2 v[64:65], v[42:43], off offset:512 nt
	global_load_dwordx2 v[66:67], v[46:47], off offset:512 nt
	s_andn2_b64 vcc, exec, s[14:15]
	s_cbranch_vccnz .LBB0_1229
